# route: router-MFMA stage renamed off the row registers (table loads via scalar base + lane offset), all row loads of the next round issued right after the stage's last table load; stacked
# speedup vs baseline: 1.0017x; 1.0017x over previous
.LBB0_583:
	s_cmp_lt_i32 s30, 5
	s_cselect_b64 s[2:3], -1, 0
	s_add_u32 s52, s28, 0x100000
	s_addc_u32 s53, s29, 0
	s_add_u32 s90, s28, 0x110000
	s_addc_u32 s91, s29, 0
	s_add_u32 s84, s28, 0x130000
	s_addc_u32 s85, s29, 0
	s_and_b64 s[44:45], s[2:3], s[0:1]
	s_andn2_b64 vcc, exec, s[44:45]
	s_cbranch_vccnz .LBB0_607
	s_cmpk_gt_i32 s93, 0xff
	s_cbranch_scc1 .LBB0_607
	v_readlane_b32 s0, v254, 12
	v_and_b32_e32 v5, 63, v0
	v_readlane_b32 s0, v254, 0
	s_andn2_b32 s0, s0, 63
	v_lshrrev_b32_e32 v1, 4, v5
	v_readlane_b32 s1, v254, 13
	v_or_b32_e32 v2, s0, v1
	v_mov_b32_e32 v125, 0
	v_mad_i64_i32 v[2:3], s[0:1], v2, 48, 0
	v_lshlrev_b32_e32 v122, 5, v5
	v_mov_b32_e32 v123, v125
	v_readlane_b32 s6, v254, 18
	v_readlane_b32 s14, v254, 26
	v_readlane_b32 s15, v254, 27
	v_and_b32_e32 v4, 15, v0
	v_readlane_b32 s0, v254, 10
	v_lshl_add_u64 v[18:19], s[14:15], 0, v[122:123]
	v_or_b32_e32 v2, v2, v4
	v_readlane_b32 s1, v254, 11
	v_readlane_b32 s6, v254, 8
	s_movk_i32 s34, 0x1000
	v_readlane_b32 s3, v254, 15
	s_mov_b64 s[46:47], 0x1000
	s_mov_b64 s[48:49], 0x1800
	v_lshl_add_u64 v[126:127], v[2:3], 4, s[0:1]
	s_nop 3
	v_readfirstlane_b32 s94, v126
	v_readfirstlane_b32 s95, v127
	s_nop 3
	v_subrev_u32_e32 v255, s94, v126
	s_lshl_b32 s0, s6, 10
	v_add_co_u32_e32 v22, vcc, s34, v18
	v_lshl_add_u64 v[26:27], v[18:19], 0, s[46:47]
	v_lshl_add_u64 v[30:31], v[18:19], 0, s[48:49]
	v_mul_u32_u24_e32 v2, 0x2010, v4
	s_add_i32 s0, s0, 0
	v_and_b32_e32 v3, 48, v5
	s_add_i32 s3, 0, 0x20100
	v_addc_co_u32_e32 v23, vcc, 0, v19, vcc
	v_lshl_add_u64 v[128:129], s[50:51], 0, v[122:123]
	v_lshlrev_b32_e32 v124, 4, v5
	v_add3_u32 v123, s0, v2, v3
	s_waitcnt vmcnt(0)
	v_lshl_add_u32 v34, v4, 2, s3
	v_cmp_eq_u32_e64 s[0:1], 0, v5
	global_load_dwordx4 v[2:5], v122, s[14:15] offset:16
	global_load_dwordx4 v[6:9], v122, s[14:15]
	global_load_dwordx4 v[10:13], v122, s[14:15] offset:2064
	global_load_dwordx4 v[14:17], v122, s[14:15] offset:2048
	global_load_dwordx4 v[18:21], v[22:23], off
	s_nop 0
	global_load_dwordx4 v[22:25], v[22:23], off offset:2048
	s_nop 0
	global_load_dwordx4 v[26:29], v[26:27], off offset:16
	s_nop 0
	global_load_dwordx4 v[30:33], v[30:31], off offset:16
	v_readlane_b32 s2, v254, 14
	v_readlane_b32 s4, v254, 16
	s_lshl_b32 s2, s6, 1
	s_mul_i32 s4, s6, 0x4020
	s_or_b32 s27, s2, 1
	v_readlane_b32 s5, v254, 17
	s_add_i32 s26, s4, 0
	s_mul_i32 s4, s27, 0x2010
	s_add_i32 s33, s4, 0
	s_mov_b64 s[4:5], 0x1900
	v_lshl_add_u64 v[134:135], v[126:127], 0, s[4:5]
	s_mov_b64 s[4:5], 0x1a00
	v_lshl_add_u64 v[136:137], v[126:127], 0, s[4:5]
	s_mov_b64 s[4:5], 0x2400
	v_lshl_add_u64 v[138:139], v[126:127], 0, s[4:5]
	s_mov_b64 s[4:5], 0x2500
	v_lshl_add_u64 v[140:141], v[126:127], 0, s[4:5]
	s_mov_b64 s[4:5], 0x2600
	v_lshl_add_u64 v[142:143], v[126:127], 0, s[4:5]
	s_mov_b64 s[4:5], 0x3000
	v_lshl_add_u64 v[144:145], v[126:127], 0, s[4:5]
	s_mov_b64 s[4:5], 0x3100
	v_lshl_add_u64 v[146:147], v[126:127], 0, s[4:5]
	s_mov_b64 s[4:5], 0x3200
	v_lshl_add_u64 v[148:149], v[126:127], 0, s[4:5]
	s_mov_b64 s[4:5], 0x3c00
	v_lshl_add_u64 v[150:151], v[126:127], 0, s[4:5]
	s_mov_b64 s[4:5], 0x3d00
	v_lshl_add_u64 v[152:153], v[126:127], 0, s[4:5]
	s_mov_b64 s[4:5], 0x3e00
	v_lshl_add_u64 v[154:155], v[126:127], 0, s[4:5]
	s_mov_b64 s[4:5], 0x4800
	v_lshl_add_u64 v[156:157], v[126:127], 0, s[4:5]
	s_mov_b64 s[4:5], 0x4900
	v_lshl_add_u64 v[158:159], v[126:127], 0, s[4:5]
	s_mov_b64 s[4:5], 0x4a00
	v_lshl_add_u64 v[160:161], v[126:127], 0, s[4:5]
	s_mov_b64 s[4:5], 0x5400
	v_lshl_add_u64 v[162:163], v[126:127], 0, s[4:5]
	s_mov_b64 s[4:5], 0x5500
	v_lshl_add_u64 v[164:165], v[126:127], 0, s[4:5]
	s_mov_b64 s[4:5], 0x5600
	v_lshl_add_u64 v[166:167], v[126:127], 0, s[4:5]
	s_mov_b64 s[4:5], 0x6000
	v_lshl_add_u64 v[168:169], v[126:127], 0, s[4:5]
	s_mov_b64 s[4:5], 0x6100
	v_lshl_add_u64 v[170:171], v[126:127], 0, s[4:5]
	s_mov_b64 s[4:5], 0x6200
	v_lshl_add_u64 v[172:173], v[126:127], 0, s[4:5]
	s_mov_b64 s[4:5], 0x6c00
	v_lshl_add_u64 v[174:175], v[126:127], 0, s[4:5]
	s_mov_b64 s[4:5], 0x6d00
	v_lshl_add_u64 v[176:177], v[126:127], 0, s[4:5]
	s_mov_b64 s[4:5], 0x6e00
	v_lshl_add_u64 v[178:179], v[126:127], 0, s[4:5]
	s_mov_b64 s[4:5], 0x7800
	v_lshl_add_u64 v[180:181], v[126:127], 0, s[4:5]
	s_mov_b64 s[4:5], 0x7900
	v_lshl_add_u64 v[182:183], v[126:127], 0, s[4:5]
	s_mov_b64 s[4:5], 0x7a00
	v_lshl_add_u64 v[184:185], v[126:127], 0, s[4:5]
	s_mov_b64 s[4:5], 0x8400
	v_lshl_add_u64 v[186:187], v[126:127], 0, s[4:5]
	s_mov_b64 s[4:5], 0x8500
	v_lshl_add_u64 v[188:189], v[126:127], 0, s[4:5]
	s_mov_b64 s[4:5], 0x8600
	v_lshl_add_u64 v[190:191], v[126:127], 0, s[4:5]
	s_mov_b64 s[4:5], 0x9000
	v_lshl_add_u64 v[192:193], v[126:127], 0, s[4:5]
	s_mov_b64 s[4:5], 0x9100
	v_lshl_add_u64 v[194:195], v[126:127], 0, s[4:5]
	s_mov_b64 s[4:5], 0x9200
	v_lshl_add_u64 v[196:197], v[126:127], 0, s[4:5]
	s_mov_b64 s[4:5], 0x9c00
	v_lshl_add_u64 v[198:199], v[126:127], 0, s[4:5]
	s_mov_b64 s[4:5], 0x9d00
	v_lshl_add_u64 v[200:201], v[126:127], 0, s[4:5]
	s_mov_b64 s[4:5], 0x9e00
	v_lshl_add_u64 v[202:203], v[126:127], 0, s[4:5]
	s_mov_b64 s[4:5], 0xa800
	v_lshl_add_u64 v[204:205], v[126:127], 0, s[4:5]
	s_mov_b64 s[4:5], 0xa900
	v_lshl_add_u64 v[206:207], v[126:127], 0, s[4:5]
	s_mov_b64 s[4:5], 0xaa00
	v_lshl_add_u64 v[208:209], v[126:127], 0, s[4:5]
	s_mov_b64 s[4:5], 0xb400
	v_lshl_add_u64 v[210:211], v[126:127], 0, s[4:5]
	s_mov_b64 s[4:5], 0xb500
	v_lshlrev_b32_e32 v1, 2, v1
	v_lshl_add_u64 v[212:213], v[126:127], 0, s[4:5]
	s_mov_b64 s[4:5], 0xb600
	v_lshl_or_b32 v1, s6, 4, v1
	v_lshl_add_u64 v[214:215], v[126:127], 0, s[4:5]
	s_movk_i32 s4, 0xc0
	v_mul_lo_u32 v1, v1, s4
	s_mul_i32 s4, s6, 0x140
	s_add_i32 s35, 0, 0x26100
	s_add_i32 s40, s35, s4
	s_mul_i32 s4, s27, 0xa0
	v_readlane_b32 s10, v254, 22
	v_readlane_b32 s11, v254, 23
	s_add_i32 s41, s35, s4
	s_movk_i32 s4, 0x240
	s_add_i32 s6, 0, 0x26b00
	v_mbcnt_lo_u32_b32 v35, -1, 0
	v_lshl_add_u64 v[130:131], s[36:37], 0, v[124:125]
	v_lshl_add_u64 v[132:133], v[126:127], 0, s[48:49]
	v_cmp_gt_u32_e64 s[10:11], 32, v0
	v_cmp_gt_u32_e64 s[4:5], s4, v0
	v_lshl_add_u32 v219, v0, 2, s6
	v_mbcnt_hi_u32_b32 v220, -1, v35
	v_mov_b32_e32 v221, 0x358637bd
	s_mov_b32 s56, 0xf800000
	v_mov_b32_e32 v222, 0x260
	v_add_u32_e32 v223, v34, v1
	s_mov_b32 s57, 0xe38f
	s_mov_b32 s62, 0xff61b1e6
	v_mov_b32_e32 v224, 0xff61b1e6
	v_readlane_b32 s7, v254, 19
	v_readlane_b32 s8, v254, 20
	v_readlane_b32 s9, v254, 21
	v_readlane_b32 s12, v254, 24
	v_readlane_b32 s13, v254, 25
	v_mov_b32_e32 v40, v0
	v_mov_b32_e32 v45, 0
	v_mul_u32_u24_sdwa v41, v40, s57 dst_sel:DWORD dst_unused:UNUSED_PAD src0_sel:WORD_0 src1_sel:DWORD
	v_lshrrev_b32_e32 v41, 21, v41
	v_mul_lo_u16_e32 v42, 36, v41
	v_sub_u16_e32 v42, v40, v42
	v_lshlrev_b32_e32 v44, 2, v42
	v_lshl_add_u64 v[38:39], s[42:43], 0, v[44:45]
	v_lshl_add_u64 v[36:37], s[38:39], 0, v[44:45]
	v_lshl_add_u64 v[38:39], v[38:39], 0, -16
	v_cmp_gt_u16_e32 vcc, 4, v42
	s_nop 1
	v_cndmask_b32_e32 v37, v39, v37, vcc
	v_cndmask_b32_e32 v36, v38, v36, vcc
	global_load_dword v42, v[36:37], off
	v_lshlrev_b32_e32 v43, 2, v40
	v_add_u32_e32 v43, 0x26c00, v43
	s_waitcnt vmcnt(0)
	ds_write_b32 v43, v42
	v_add_u32_e32 v40, 0x200, v40
	v_cmp_gt_u32_e32 vcc, 0x240, v40
	s_and_saveexec_b64 s[14:15], vcc
	v_mul_u32_u24_sdwa v41, v40, s57 dst_sel:DWORD dst_unused:UNUSED_PAD src0_sel:WORD_0 src1_sel:DWORD
	v_lshrrev_b32_e32 v41, 21, v41
	v_mul_lo_u16_e32 v42, 36, v41
	v_sub_u16_e32 v42, v40, v42
	v_lshlrev_b32_e32 v44, 2, v42
	v_lshl_add_u64 v[38:39], s[42:43], 0, v[44:45]
	v_lshl_add_u64 v[36:37], s[38:39], 0, v[44:45]
	v_lshl_add_u64 v[38:39], v[38:39], 0, -16
	v_cmp_gt_u16_e32 vcc, 4, v42
	s_nop 1
	v_cndmask_b32_e32 v37, v39, v37, vcc
	v_cndmask_b32_e32 v36, v38, v36, vcc
	global_load_dword v42, v[36:37], off
	v_lshlrev_b32_e32 v43, 2, v40
	v_add_u32_e32 v43, 0x26c00, v43
	s_waitcnt vmcnt(0)
	ds_write_b32 v43, v42
	s_or_b64 exec, exec, s[14:15]
	s_branch .LBB0_587

.LBB0_587:
	s_and_saveexec_b64 s[6:7], s[10:11]
	ds_write_b32 v219, v125
	s_or_b64 exec, exec, s[6:7]
	s_lshl_b32 s66, s93, 6
	s_add_i32 s67, s66, s2
	s_mov_b32 s68, 0
	s_waitcnt lgkmcnt(0)
	s_barrier
	s_mov_b32 s82, 0
	s_lshl_b32 s82, s82, 4
	s_add_i32 s82, s67, s82
	s_ashr_i32 s83, s82, 31
	s_lshl_b64 s[82:83], s[82:83], 13
	v_lshl_add_u64 v[98:99], v[128:129], 0, s[82:83]
	s_add_u32 s82, s82, 0x1000
	s_addc_u32 s83, s83, 0
	global_load_dwordx4 v[118:121], v[98:99], off
	global_load_dwordx4 v[114:117], v[98:99], off offset:16
	global_load_dwordx4 v[110:113], v[98:99], off offset:2048
	global_load_dwordx4 v[106:109], v[98:99], off offset:2064
	v_lshl_add_u64 v[100:101], v[128:129], 0, s[82:83]
	s_add_u32 s82, s82, 0x1000
	s_addc_u32 s83, s83, 0
	global_load_dwordx4 v[58:61], v[100:101], off offset:2064
	global_load_dwordx4 v[90:93], v[100:101], off
	global_load_dwordx4 v[66:69], v[100:101], off offset:16
	global_load_dwordx4 v[62:65], v[100:101], off offset:2048
	v_lshl_add_u64 v[98:99], v[128:129], 0, s[82:83]
	s_nop 0
	global_load_dwordx4 v[54:57], v[98:99], off
	global_load_dwordx4 v[50:53], v[98:99], off offset:16
	global_load_dwordx4 v[196:199], v[98:99], off offset:2064
	global_load_dwordx4 v[200:203], v[98:99], off offset:2048
	s_add_u32 s82, s82, 0x1000
	s_addc_u32 s83, s83, 0
	v_lshl_add_u64 v[100:101], v[128:129], 0, s[82:83]
	s_nop 0
	global_load_dwordx4 v[204:207], v[100:101], off
	global_load_dwordx4 v[208:211], v[100:101], off offset:16
	global_load_dwordx4 v[102:105], v[100:101], off offset:2048
	global_load_dwordx4 v[212:215], v[100:101], off offset:2064
	s_branch .LBB0_592

.LBB0_592:
	s_lshl_b32 s8, s68, 4
	s_add_i32 s6, s67, s8
	s_ashr_i32 s7, s6, 31
	s_lshl_b64 s[12:13], s[6:7], 13
	v_lshl_add_u64 v[34:35], v[128:129], 0, s[12:13]
	v_lshl_add_u64 v[36:37], v[34:35], 0, s[48:49]
	v_add_co_u32_e32 v36, vcc, 0x1000, v34
	v_and_b32_e32 v1, 64, v220
	s_nop 0
	v_addc_co_u32_e32 v37, vcc, 0, v35, vcc
	v_lshl_add_u64 v[34:35], v[34:35], 0, s[46:47]
	v_xor_b32_e32 v34, 1, v220
	v_add_u32_e32 v1, 64, v1
	s_or_b32 s6, s6, 1
	v_cmp_lt_i32_e32 vcc, v34, v1
	s_ashr_i32 s7, s6, 31
	s_lshl_b64 s[6:7], s[6:7], 13
	v_cndmask_b32_e32 v34, v220, v34, vcc
	v_lshlrev_b32_e32 v218, 2, v34
	v_lshl_add_u64 v[34:35], v[128:129], 0, s[6:7]
	v_add_co_u32_e32 v70, vcc, s34, v34
	v_lshl_add_u64 v[36:37], v[34:35], 0, s[46:47]
	s_nop 0
	v_addc_co_u32_e32 v71, vcc, 0, v35, vcc
	v_lshl_add_u64 v[72:73], v[34:35], 0, s[48:49]
	s_nop 0
	s_add_i32 s8, s8, s66
	s_add_i32 s54, s8, s2
	s_ashr_i32 s55, s54, 31
	s_add_i32 s58, s8, s27
	s_ashr_i32 s59, s58, 31
	s_waitcnt vmcnt(13)
	v_mov_b32_e32 v76, v119
	s_waitcnt vmcnt(12)
	v_mov_b32_e32 v77, v115
	v_mov_b32_e32 v80, v121
	v_mov_b32_e32 v81, v117
	v_mov_b32_e32 v74, v118
	v_mov_b32_e32 v75, v114
	v_mov_b32_e32 v78, v120
	v_mov_b32_e32 v79, v116
	s_waitcnt vmcnt(11)
	v_pk_mul_f32 v[82:83], v[112:113], v[112:113]
	v_pk_mul_f32 v[84:85], v[110:111], v[110:111]
	v_pk_mul_f32 v[76:77], v[76:77], v[76:77]
	v_pk_mul_f32 v[80:81], v[80:81], v[80:81]
	v_pk_mov_b32 v[94:95], v[84:85], v[82:83] op_sel:[1,0]
	v_mov_b32_e32 v85, v83
	v_pk_fma_f32 v[74:75], v[74:75], v[74:75], v[76:77]
	v_pk_fma_f32 v[76:77], v[78:79], v[78:79], v[80:81]
	s_waitcnt vmcnt(10)
	v_mul_f32_e32 v86, v107, v107
	v_mul_f32_e32 v88, v109, v109
	v_pk_add_f32 v[78:79], v[94:95], v[84:85]
	v_pk_add_f32 v[74:75], v[74:75], v[76:77]
	v_pk_fma_f32 v[82:83], v[106:107], v[106:107], v[86:87] op_sel_hi:[1,1,0]
	v_pk_fma_f32 v[86:87], v[108:109], v[108:109], v[88:89] op_sel_hi:[1,1,0]
	s_waitcnt vmcnt(8)
	v_mul_f32_e32 v95, v90, v90
	v_mul_f32_e32 v100, v91, v91
	v_pk_add_f32 v[76:77], v[78:79], v[78:79] op_sel:[0,1] op_sel_hi:[1,0]
	v_pk_add_f32 v[74:75], v[74:75], v[74:75] op_sel:[0,1] op_sel_hi:[1,0]
	v_mul_f32_e32 v83, v92, v92
	v_mul_f32_e32 v87, v93, v93
	s_waitcnt vmcnt(7)
	v_pk_mul_f32 v[80:81], v[68:69], v[68:69]
	v_pk_mul_f32 v[84:85], v[66:67], v[66:67]
	v_mov_b32_e32 v77, v100
	v_mov_b32_e32 v75, v95
	v_pk_mov_b32 v[78:79], v[84:85], v[80:81] op_sel:[1,0]
	v_mov_b32_e32 v85, v81
	v_pk_add_f32 v[82:83], v[82:83], v[86:87]
	v_pk_add_f32 v[74:75], v[74:75], v[76:77]
	s_waitcnt vmcnt(6)
	v_mul_f32_e32 v88, v63, v63
	v_mul_f32_e32 v94, v65, v65
	v_pk_add_f32 v[78:79], v[78:79], v[84:85]
	v_pk_add_f32 v[74:75], v[74:75], v[82:83]
	v_mul_f32_e32 v96, v58, v58
	v_mul_f32_e32 v97, v59, v59
	v_mul_f32_e32 v98, v60, v60
	v_mul_f32_e32 v99, v61, v61
	v_pk_fma_f32 v[80:81], v[62:63], v[62:63], v[88:89] op_sel_hi:[1,1,0]
	v_pk_fma_f32 v[88:89], v[64:65], v[64:65], v[94:95] op_sel_hi:[1,1,0]
	v_pk_add_f32 v[78:79], v[78:79], v[78:79] op_sel:[0,1] op_sel_hi:[1,0]
	v_pk_add_f32 v[74:75], v[74:75], v[74:75] op_sel:[0,1] op_sel_hi:[1,0]
	v_mov_b32_e32 v81, v98
	v_mov_b32_e32 v79, v97
	v_mov_b32_e32 v75, v96
	v_mov_b32_e32 v89, v99
	v_pk_add_f32 v[74:75], v[74:75], v[78:79]
	v_pk_add_f32 v[76:77], v[80:81], v[88:89]
	s_waitcnt vmcnt(0)
	v_mov_b32_e32 v42, v196
	v_mov_b32_e32 v43, v197
	v_mov_b32_e32 v44, v198
	v_mov_b32_e32 v45, v199
	v_mov_b32_e32 v46, v200
	v_mov_b32_e32 v47, v201
	v_mov_b32_e32 v48, v202
	v_mov_b32_e32 v49, v203
	v_mov_b32_e32 v38, v204
	v_mov_b32_e32 v39, v205
	v_mov_b32_e32 v40, v206
	v_mov_b32_e32 v41, v207
	v_mov_b32_e32 v34, v208
	v_mov_b32_e32 v35, v209
	v_mov_b32_e32 v36, v210
	v_mov_b32_e32 v37, v211
	v_mov_b32_e32 v98, v212
	v_mov_b32_e32 v99, v213
	v_mov_b32_e32 v100, v214
	v_mov_b32_e32 v101, v215
	global_load_dwordx4 v[82:85], v[126:127], off
	global_load_dwordx4 v[86:89], v[126:127], off offset:256
	v_pk_add_f32 v[74:75], v[74:75], v[76:77]
	v_xor_b32_e32 v76, 2, v220
	v_add_f32_e32 v74, v74, v75
	ds_bpermute_b32 v75, v218, v74
	v_cmp_lt_i32_e32 vcc, v76, v1
	s_waitcnt lgkmcnt(0)
	v_add_f32_e32 v74, v74, v75
	v_cndmask_b32_e32 v76, v220, v76, vcc
	v_lshlrev_b32_e32 v225, 2, v76
	ds_bpermute_b32 v75, v225, v74
	v_xor_b32_e32 v76, 4, v220
	v_cmp_lt_i32_e32 vcc, v76, v1
	s_waitcnt lgkmcnt(0)
	v_add_f32_e32 v74, v74, v75
	v_cndmask_b32_e32 v76, v220, v76, vcc
	v_lshlrev_b32_e32 v230, 2, v76
	ds_bpermute_b32 v75, v230, v74
	v_xor_b32_e32 v76, 8, v220
	v_cmp_lt_i32_e32 vcc, v76, v1
	s_waitcnt lgkmcnt(0)
	v_add_f32_e32 v74, v74, v75
	v_cndmask_b32_e32 v76, v220, v76, vcc
	v_lshlrev_b32_e32 v231, 2, v76
	ds_bpermute_b32 v75, v231, v74
	v_xor_b32_e32 v76, 16, v220
	v_cmp_lt_i32_e32 vcc, v76, v1
	s_waitcnt lgkmcnt(0)
	v_add_f32_e32 v74, v74, v75
	v_cndmask_b32_e32 v76, v220, v76, vcc
	v_lshlrev_b32_e32 v232, 2, v76
	ds_bpermute_b32 v75, v232, v74
	v_xor_b32_e32 v76, 32, v220
	v_cmp_lt_i32_e32 vcc, v76, v1
	s_waitcnt lgkmcnt(0)
	v_add_f32_e32 v74, v74, v75
	v_cndmask_b32_e32 v1, v220, v76, vcc
	v_lshlrev_b32_e32 v1, 2, v1
	ds_bpermute_b32 v75, v1, v74
	s_waitcnt lgkmcnt(0)
	v_add_f32_e32 v70, v74, v75
	v_fmamk_f32 v70, v70, 0x3a000000, v221
	v_mul_f32_e32 v71, 0x4f800000, v70
	v_cmp_gt_f32_e32 vcc, s56, v70
	s_nop 1
	v_cndmask_b32_e32 v124, v70, v71, vcc
	v_sqrt_f32_e32 v216, v124
	global_load_dwordx4 v[94:97], v[126:127], off offset:512
	global_load_dwordx4 v[70:73], v[126:127], off offset:3072
	global_load_dwordx4 v[74:77], v[126:127], off offset:3328
	global_load_dwordx4 v[78:81], v[126:127], off offset:3584
	v_add_u32_e32 v217, -1, v216
	v_fma_f32 v226, -v217, v216, v124
	v_cmp_ge_f32_e64 s[6:7], 0, v226
	v_add_u32_e32 v226, 1, v216
	s_nop 0
	v_cndmask_b32_e64 v217, v216, v217, s[6:7]
	v_fma_f32 v216, -v226, v216, v124
	v_cmp_lt_f32_e64 s[6:7], 0, v216
	s_nop 1
	v_cndmask_b32_e64 v216, v217, v226, s[6:7]
	v_mul_f32_e32 v217, 0x37800000, v216
	v_cndmask_b32_e32 v216, v216, v217, vcc
	v_cmp_class_f32_e32 vcc, v124, v222
	s_nop 1
	v_cndmask_b32_e32 v124, v216, v124, vcc
	v_div_scale_f32 v216, s[6:7], v124, v124, 1.0
	v_rcp_f32_e32 v217, v216
	s_lshl_b64 s[6:7], s[54:55], 12
	v_fma_f32 v226, -v216, v217, 1.0
	v_fmac_f32_e32 v217, v226, v217
	v_div_scale_f32 v226, vcc, 1.0, v124, 1.0
	v_mul_f32_e32 v227, v226, v217
	v_fma_f32 v228, -v216, v227, v226
	v_fmac_f32_e32 v227, v228, v217
	v_fma_f32 v216, -v216, v227, v226
	v_div_fmas_f32 v216, v216, v217, v227
	v_div_fixup_f32 v124, v216, v124, 1.0
	v_pk_mul_f32 v[118:119], v[118:119], v[124:125] op_sel_hi:[1,0]
	v_pk_mul_f32 v[120:121], v[120:121], v[124:125] op_sel_hi:[1,0]
	v_pk_mul_f32 v[114:115], v[114:115], v[124:125] op_sel_hi:[1,0]
	v_pk_mul_f32 v[116:117], v[116:117], v[124:125] op_sel_hi:[1,0]
	v_pk_mul_f32 v[120:121], v[8:9], v[120:121]
	v_pk_mul_f32 v[118:119], v[6:7], v[118:119]
	v_pk_mul_f32 v[116:117], v[4:5], v[116:117]
	v_pk_mul_f32 v[114:115], v[2:3], v[114:115]
	v_lshl_add_u64 v[216:217], v[130:131], 0, s[6:7]
	v_cvt_pk_bf16_f32 v226, v118, v119
	v_cvt_pk_bf16_f32 v227, v120, v121
	v_cvt_pk_bf16_f32 v228, v114, v115
	v_cvt_pk_bf16_f32 v229, v116, v117
	v_pk_mul_f32 v[110:111], v[110:111], v[124:125] op_sel_hi:[1,0]
	v_pk_mul_f32 v[112:113], v[112:113], v[124:125] op_sel_hi:[1,0]
	v_pk_mul_f32 v[106:107], v[106:107], v[124:125] op_sel_hi:[1,0]
	v_pk_mul_f32 v[108:109], v[108:109], v[124:125] op_sel_hi:[1,0]
	global_store_dwordx4 v[216:217], v[226:229], off
	v_pk_mul_f32 v[112:113], v[16:17], v[112:113]
	v_pk_mul_f32 v[110:111], v[14:15], v[110:111]
	v_add_u32_e32 v226, s26, v122
	v_pk_mul_f32 v[108:109], v[12:13], v[108:109]
	v_pk_mul_f32 v[106:107], v[10:11], v[106:107]
	ds_write_b128 v226, v[118:121]
	ds_write_b128 v226, v[114:117] offset:16
	v_cvt_pk_bf16_f32 v114, v110, v111
	v_cvt_pk_bf16_f32 v115, v112, v113
	v_cvt_pk_bf16_f32 v116, v106, v107
	v_cvt_pk_bf16_f32 v117, v108, v109
	global_store_dwordx4 v[216:217], v[114:117], off offset:1024
	ds_write_b128 v226, v[110:113] offset:2048
	ds_write_b128 v226, v[106:109] offset:2064
	s_waitcnt vmcnt(15)
	v_mov_b32_e32 v108, v55
	s_waitcnt vmcnt(14)
	v_mov_b32_e32 v109, v51
	v_mov_b32_e32 v106, v54
	v_mov_b32_e32 v107, v50
	v_pk_mul_f32 v[108:109], v[108:109], v[108:109]
	v_mov_b32_e32 v110, v57
	v_mov_b32_e32 v111, v53
	v_pk_fma_f32 v[106:107], v[106:107], v[106:107], v[108:109]
	v_mov_b32_e32 v108, v56
	v_mov_b32_e32 v109, v52
	v_pk_mul_f32 v[110:111], v[110:111], v[110:111]
	v_pk_mul_f32 v[90:91], v[90:91], v[124:125] op_sel_hi:[1,0]
	v_pk_fma_f32 v[108:109], v[108:109], v[108:109], v[110:111]
	s_waitcnt vmcnt(12)
	v_pk_mul_f32 v[110:111], v[46:47], v[46:47]
	v_pk_add_f32 v[106:107], v[106:107], v[108:109]
	v_pk_mul_f32 v[108:109], v[48:49], v[48:49]
	v_pk_add_f32 v[106:107], v[106:107], v[106:107] op_sel:[0,1] op_sel_hi:[1,0]
	v_pk_mov_b32 v[112:113], v[110:111], v[108:109] op_sel:[1,0]
	v_mov_b32_e32 v111, v109
	v_pk_add_f32 v[108:109], v[112:113], v[110:111]
	s_waitcnt vmcnt(11)
	v_mul_f32_e32 v110, v38, v38
	v_mul_f32_e32 v111, v39, v39
	v_pk_add_f32 v[108:109], v[108:109], v[108:109] op_sel:[0,1] op_sel_hi:[1,0]
	v_mov_b32_e32 v107, v110
	v_mov_b32_e32 v109, v111
	v_pk_add_f32 v[106:107], v[106:107], v[108:109]
	v_mul_f32_e32 v108, v43, v43
	v_mul_f32_e32 v110, v45, v45
	v_mul_f32_e32 v112, v40, v40
	v_mul_f32_e32 v113, v41, v41
	v_pk_fma_f32 v[108:109], v[42:43], v[42:43], v[108:109] op_sel_hi:[1,1,0]
	v_pk_fma_f32 v[110:111], v[44:45], v[44:45], v[110:111] op_sel_hi:[1,1,0]
	v_mov_b32_e32 v109, v112
	v_mov_b32_e32 v111, v113
	v_pk_add_f32 v[108:109], v[108:109], v[110:111]
	s_waitcnt vmcnt(10)
	v_pk_mul_f32 v[110:111], v[34:35], v[34:35]
	v_pk_add_f32 v[106:107], v[106:107], v[108:109]
	v_pk_mul_f32 v[108:109], v[36:37], v[36:37]
	v_pk_add_f32 v[106:107], v[106:107], v[106:107] op_sel:[0,1] op_sel_hi:[1,0]
	v_pk_mov_b32 v[112:113], v[110:111], v[108:109] op_sel:[1,0]
	v_mov_b32_e32 v111, v109
	v_pk_add_f32 v[108:109], v[112:113], v[110:111]
	s_waitcnt vmcnt(8)
	v_mul_f32_e32 v110, v98, v98
	v_mul_f32_e32 v111, v99, v99
	v_pk_add_f32 v[108:109], v[108:109], v[108:109] op_sel:[0,1] op_sel_hi:[1,0]
	v_mov_b32_e32 v107, v110
	v_mov_b32_e32 v109, v111
	v_pk_add_f32 v[106:107], v[106:107], v[108:109]
	v_mul_f32_e32 v108, v103, v103
	v_mul_f32_e32 v110, v105, v105
	v_mul_f32_e32 v112, v100, v100
	v_mul_f32_e32 v113, v101, v101
	v_pk_fma_f32 v[108:109], v[102:103], v[102:103], v[108:109] op_sel_hi:[1,1,0]
	v_pk_fma_f32 v[110:111], v[104:105], v[104:105], v[110:111] op_sel_hi:[1,1,0]
	v_mov_b32_e32 v109, v112
	v_mov_b32_e32 v111, v113
	v_pk_add_f32 v[108:109], v[108:109], v[110:111]
	v_pk_mul_f32 v[92:93], v[92:93], v[124:125] op_sel_hi:[1,0]
	v_pk_add_f32 v[106:107], v[106:107], v[108:109]
	v_pk_mul_f32 v[66:67], v[66:67], v[124:125] op_sel_hi:[1,0]
	v_add_f32_e32 v106, v106, v107
	ds_bpermute_b32 v107, v218, v106
	v_pk_mul_f32 v[68:69], v[68:69], v[124:125] op_sel_hi:[1,0]
	v_pk_mul_f32 v[92:93], v[20:21], v[92:93]
	v_pk_mul_f32 v[90:91], v[18:19], v[90:91]
	v_pk_mul_f32 v[68:69], v[28:29], v[68:69]
	s_waitcnt lgkmcnt(0)
	v_add_f32_e32 v107, v106, v107
	ds_bpermute_b32 v108, v225, v107
	v_pk_mul_f32 v[66:67], v[26:27], v[66:67]
	v_cvt_pk_bf16_f32 v106, v90, v91
	v_cvt_pk_bf16_f32 v109, v68, v69
	v_pk_mul_f32 v[62:63], v[62:63], v[124:125] op_sel_hi:[1,0]
	s_waitcnt lgkmcnt(0)
	v_add_f32_e32 v110, v107, v108
	ds_bpermute_b32 v111, v230, v110
	v_cvt_pk_bf16_f32 v107, v92, v93
	v_cvt_pk_bf16_f32 v108, v66, v67
	global_store_dwordx4 v[216:217], v[106:109], off offset:2048
	ds_write_b128 v226, v[90:93] offset:4096
	ds_write_b128 v226, v[66:69] offset:4112
	s_waitcnt lgkmcnt(2)
	v_add_f32_e32 v106, v110, v111
	ds_bpermute_b32 v107, v231, v106
	v_pk_mul_f32 v[64:65], v[64:65], v[124:125] op_sel_hi:[1,0]
	v_pk_mul_f32 v[58:59], v[58:59], v[124:125] op_sel_hi:[1,0]
	v_pk_mul_f32 v[60:61], v[60:61], v[124:125] op_sel_hi:[1,0]
	v_pk_mul_f32 v[64:65], v[24:25], v[64:65]
	s_waitcnt lgkmcnt(0)
	v_add_f32_e32 v66, v106, v107
	ds_bpermute_b32 v67, v232, v66
	v_pk_mul_f32 v[62:63], v[22:23], v[62:63]
	v_pk_mul_f32 v[60:61], v[32:33], v[60:61]
	v_pk_mul_f32 v[58:59], v[30:31], v[58:59]
	v_cvt_pk_bf16_f32 v69, v60, v61
	s_waitcnt lgkmcnt(0)
	v_add_f32_e32 v68, v66, v67
	ds_bpermute_b32 v1, v1, v68
	v_cvt_pk_bf16_f32 v66, v62, v63
	v_cvt_pk_bf16_f32 v67, v64, v65
	s_waitcnt lgkmcnt(0)
	v_add_f32_e32 v1, v68, v1
	v_fmamk_f32 v1, v1, 0x3a000000, v221
	v_mul_f32_e32 v68, 0x4f800000, v1
	v_cmp_gt_f32_e32 vcc, s56, v1
	s_nop 1
	v_cndmask_b32_e32 v1, v1, v68, vcc
	v_sqrt_f32_e32 v90, v1
	v_cvt_pk_bf16_f32 v68, v58, v59
	global_store_dwordx4 v[216:217], v[66:69], off offset:3072
	ds_write_b128 v226, v[62:65] offset:6144
	ds_write_b128 v226, v[58:61] offset:6160
	v_add_u32_e32 v66, -1, v90
	v_fma_f32 v67, -v66, v90, v1
	v_cmp_ge_f32_e64 s[6:7], 0, v67
	v_add_u32_e32 v67, 1, v90
	v_fma_f32 v68, -v67, v90, v1
	v_cndmask_b32_e64 v66, v90, v66, s[6:7]
	v_cmp_lt_f32_e64 s[6:7], 0, v68
	s_nop 1
	v_cndmask_b32_e64 v66, v66, v67, s[6:7]
	v_mul_f32_e32 v67, 0x37800000, v66
	v_cndmask_b32_e32 v66, v66, v67, vcc
	v_cmp_class_f32_e32 vcc, v1, v222
	s_nop 1
	v_cndmask_b32_e32 v1, v66, v1, vcc
	v_div_scale_f32 v66, s[6:7], v1, v1, 1.0
	v_rcp_f32_e32 v67, v66
	s_lshl_b64 s[6:7], s[58:59], 12
	v_lshl_add_u64 v[64:65], v[130:131], 0, s[6:7]
	v_fma_f32 v58, -v66, v67, 1.0
	v_fmac_f32_e32 v67, v58, v67
	v_div_scale_f32 v58, vcc, 1.0, v1, 1.0
	v_mul_f32_e32 v59, v58, v67
	v_fma_f32 v60, -v66, v59, v58
	v_fmac_f32_e32 v59, v60, v67
	v_fma_f32 v58, -v66, v59, v58
	v_div_fmas_f32 v58, v58, v67, v59
	v_div_fixup_f32 v62, v58, v1, 1.0
	v_pk_mul_f32 v[54:55], v[54:55], v[62:63] op_sel_hi:[1,0]
	v_pk_mul_f32 v[56:57], v[56:57], v[62:63] op_sel_hi:[1,0]
	v_pk_mul_f32 v[50:51], v[50:51], v[62:63] op_sel_hi:[1,0]
	v_pk_mul_f32 v[52:53], v[52:53], v[62:63] op_sel_hi:[1,0]
	v_pk_mul_f32 v[56:57], v[8:9], v[56:57]
	v_pk_mul_f32 v[54:55], v[6:7], v[54:55]
	v_pk_mul_f32 v[52:53], v[4:5], v[52:53]
	v_pk_mul_f32 v[50:51], v[2:3], v[50:51]
	v_pk_mul_f32 v[46:47], v[46:47], v[62:63] op_sel_hi:[1,0]
	v_pk_mul_f32 v[48:49], v[48:49], v[62:63] op_sel_hi:[1,0]
	v_pk_mul_f32 v[42:43], v[42:43], v[62:63] op_sel_hi:[1,0]
	v_pk_mul_f32 v[44:45], v[44:45], v[62:63] op_sel_hi:[1,0]
	v_cvt_pk_bf16_f32 v58, v54, v55
	v_cvt_pk_bf16_f32 v59, v56, v57
	v_cvt_pk_bf16_f32 v60, v50, v51
	v_cvt_pk_bf16_f32 v61, v52, v53
	v_add_u32_e32 v1, s33, v122
	v_pk_mul_f32 v[48:49], v[16:17], v[48:49]
	v_pk_mul_f32 v[46:47], v[14:15], v[46:47]
	v_pk_mul_f32 v[44:45], v[12:13], v[44:45]
	v_pk_mul_f32 v[42:43], v[10:11], v[42:43]
	v_pk_mul_f32 v[38:39], v[38:39], v[62:63] op_sel_hi:[1,0]
	v_pk_mul_f32 v[40:41], v[40:41], v[62:63] op_sel_hi:[1,0]
	v_pk_mul_f32 v[34:35], v[34:35], v[62:63] op_sel_hi:[1,0]
	v_pk_mul_f32 v[36:37], v[36:37], v[62:63] op_sel_hi:[1,0]
	global_store_dwordx4 v[64:65], v[58:61], off
	ds_write_b128 v1, v[54:57]
	ds_write_b128 v1, v[50:53] offset:16
	v_cvt_pk_bf16_f32 v50, v46, v47
	v_cvt_pk_bf16_f32 v51, v48, v49
	v_cvt_pk_bf16_f32 v52, v42, v43
	v_cvt_pk_bf16_f32 v53, v44, v45
	v_pk_mul_f32 v[40:41], v[20:21], v[40:41]
	v_pk_mul_f32 v[38:39], v[18:19], v[38:39]
	v_pk_mul_f32 v[36:37], v[28:29], v[36:37]
	v_pk_mul_f32 v[34:35], v[26:27], v[34:35]
	global_store_dwordx4 v[64:65], v[50:53], off offset:1024
	ds_write_b128 v1, v[46:49] offset:2048
	ds_write_b128 v1, v[42:45] offset:2064
	v_cvt_pk_bf16_f32 v42, v38, v39
	v_cvt_pk_bf16_f32 v43, v40, v41
	v_cvt_pk_bf16_f32 v44, v34, v35
	v_cvt_pk_bf16_f32 v45, v36, v37
	global_store_dwordx4 v[64:65], v[42:45], off offset:2048
	ds_write_b128 v1, v[38:41] offset:4096
	ds_write_b128 v1, v[34:37] offset:4112
	v_pk_mul_f32 v[34:35], v[102:103], v[62:63] op_sel_hi:[1,0]
	v_pk_mul_f32 v[36:37], v[104:105], v[62:63] op_sel_hi:[1,0]
	v_pk_mul_f32 v[38:39], v[98:99], v[62:63] op_sel_hi:[1,0]
	v_pk_mul_f32 v[40:41], v[100:101], v[62:63] op_sel_hi:[1,0]
	v_pk_mul_f32 v[36:37], v[24:25], v[36:37]
	v_pk_mul_f32 v[34:35], v[22:23], v[34:35]
	v_pk_mul_f32 v[40:41], v[32:33], v[40:41]
	v_pk_mul_f32 v[38:39], v[30:31], v[38:39]
	v_cvt_pk_bf16_f32 v42, v34, v35
	v_cvt_pk_bf16_f32 v43, v36, v37
	v_cvt_pk_bf16_f32 v44, v38, v39
	v_cvt_pk_bf16_f32 v45, v40, v41
	global_store_dwordx4 v[64:65], v[42:45], off offset:3072
	ds_write_b128 v1, v[34:37] offset:6144
	ds_write_b128 v1, v[38:41] offset:6160
	s_waitcnt lgkmcnt(0)
	s_barrier
	v_add_u32_e32 v216, 0x1800, v255
	global_load_dwordx4 v[132:135], v216, s[94:95]
	v_add_u32_e32 v216, 0x1900, v255
	global_load_dwordx4 v[136:139], v216, s[94:95]
	v_add_u32_e32 v216, 0x1a00, v255
	global_load_dwordx4 v[140:143], v216, s[94:95]
	v_add_u32_e32 v216, 0x2400, v255
	global_load_dwordx4 v[144:147], v216, s[94:95]
	v_add_u32_e32 v216, 0x2500, v255
	global_load_dwordx4 v[148:151], v216, s[94:95]
	v_add_u32_e32 v216, 0x2600, v255
	global_load_dwordx4 v[152:155], v216, s[94:95]
	v_add_u32_e32 v216, 0x3000, v255
	global_load_dwordx4 v[156:159], v216, s[94:95]
	v_add_u32_e32 v216, 0x3100, v255
	global_load_dwordx4 v[160:163], v216, s[94:95]
	v_add_u32_e32 v216, 0x3200, v255
	global_load_dwordx4 v[164:167], v216, s[94:95]
	v_add_u32_e32 v216, 0x3c00, v255
	global_load_dwordx4 v[168:171], v216, s[94:95]
	v_add_u32_e32 v216, 0x3d00, v255
	global_load_dwordx4 v[172:175], v216, s[94:95]
	v_add_u32_e32 v216, 0x3e00, v255
	global_load_dwordx4 v[176:179], v216, s[94:95]
	v_add_u32_e32 v216, 0x4800, v255
	global_load_dwordx4 v[180:183], v216, s[94:95]
	v_add_u32_e32 v216, 0x4900, v255
	global_load_dwordx4 v[184:187], v216, s[94:95]
	v_add_u32_e32 v216, 0x4a00, v255
	global_load_dwordx4 v[188:191], v216, s[94:95]
	v_add_u32_e32 v216, 0x5400, v255
	global_load_dwordx4 v[192:195], v216, s[94:95]
	v_add_u32_e32 v216, 0x5500, v255
	global_load_dwordx4 v[226:229], v216, s[94:95]
	v_add_u32_e32 v216, 0x5600, v255
	global_load_dwordx4 v[230:233], v216, s[94:95]
	ds_read_b128 v[234:237], v123
	ds_read_b128 v[238:241], v123 offset:64
	s_waitcnt vmcnt(31) lgkmcnt(1)
	v_mfma_f32_16x16x4_f32 v[242:245], v234, v82, 0
	s_waitcnt vmcnt(30)
	v_mfma_f32_16x16x4_f32 v[246:249], v234, v86, 0
	s_waitcnt vmcnt(29)
	v_mfma_f32_16x16x4_f32 v[250:253], v234, v94, 0
	v_mfma_f32_16x16x4_f32 v[242:245], v235, v83, v[242:245]
	v_mfma_f32_16x16x4_f32 v[246:249], v235, v87, v[246:249]
	v_mfma_f32_16x16x4_f32 v[250:253], v235, v95, v[250:253]
	v_mfma_f32_16x16x4_f32 v[242:245], v236, v84, v[242:245]
	v_mfma_f32_16x16x4_f32 v[246:249], v236, v88, v[246:249]
	v_mfma_f32_16x16x4_f32 v[250:253], v236, v96, v[250:253]
	v_mfma_f32_16x16x4_f32 v[82:85], v237, v85, v[242:245]
	v_mfma_f32_16x16x4_f32 v[86:89], v237, v89, v[246:249]
	v_mfma_f32_16x16x4_f32 v[94:97], v237, v97, v[250:253]
	s_waitcnt vmcnt(28) lgkmcnt(0)
	v_mfma_f32_16x16x4_f32 v[82:85], v238, v70, v[82:85]
	s_waitcnt vmcnt(27)
	v_mfma_f32_16x16x4_f32 v[86:89], v238, v74, v[86:89]
	s_waitcnt vmcnt(26)
	v_mfma_f32_16x16x4_f32 v[94:97], v238, v78, v[94:97]
	v_mfma_f32_16x16x4_f32 v[82:85], v239, v71, v[82:85]
	v_mfma_f32_16x16x4_f32 v[86:89], v239, v75, v[86:89]
	v_mfma_f32_16x16x4_f32 v[94:97], v239, v79, v[94:97]
	v_mfma_f32_16x16x4_f32 v[82:85], v240, v72, v[82:85]
	v_mfma_f32_16x16x4_f32 v[86:89], v240, v76, v[86:89]
	v_mfma_f32_16x16x4_f32 v[94:97], v240, v80, v[94:97]
	v_mfma_f32_16x16x4_f32 v[70:73], v241, v73, v[82:85]
	v_mfma_f32_16x16x4_f32 v[74:77], v241, v77, v[86:89]
	s_nop 5
	ds_read_b128 v[82:85], v123 offset:128
	ds_read_b128 v[86:89], v123 offset:192
	v_mfma_f32_16x16x4_f32 v[78:81], v241, v81, v[94:97]
	s_waitcnt vmcnt(17) lgkmcnt(1)
	v_mfma_f32_16x16x4_f32 v[70:73], v82, v132, v[70:73]
	s_waitcnt vmcnt(16)
	v_mfma_f32_16x16x4_f32 v[74:77], v82, v136, v[74:77]
	s_waitcnt vmcnt(15)
	v_mfma_f32_16x16x4_f32 v[78:81], v82, v140, v[78:81]
	v_mfma_f32_16x16x4_f32 v[70:73], v83, v133, v[70:73]
	v_mfma_f32_16x16x4_f32 v[74:77], v83, v137, v[74:77]
	v_mfma_f32_16x16x4_f32 v[78:81], v83, v141, v[78:81]
	v_mfma_f32_16x16x4_f32 v[70:73], v84, v134, v[70:73]
	v_mfma_f32_16x16x4_f32 v[74:77], v84, v138, v[74:77]
	v_mfma_f32_16x16x4_f32 v[78:81], v84, v142, v[78:81]
	v_mfma_f32_16x16x4_f32 v[132:135], v85, v135, v[70:73]
	v_mfma_f32_16x16x4_f32 v[136:139], v85, v139, v[74:77]
	v_mfma_f32_16x16x4_f32 v[140:143], v85, v143, v[78:81]
	s_waitcnt vmcnt(12) lgkmcnt(0)
	v_mfma_f32_16x16x4_f32 v[140:143], v86, v152, v[140:143]
	v_mfma_f32_16x16x4_f32 v[132:135], v86, v144, v[132:135]
	v_mfma_f32_16x16x4_f32 v[136:139], v86, v148, v[136:139]
	v_mfma_f32_16x16x4_f32 v[140:143], v87, v153, v[140:143]
	v_mfma_f32_16x16x4_f32 v[132:135], v87, v145, v[132:135]
	v_mfma_f32_16x16x4_f32 v[136:139], v87, v149, v[136:139]
	v_mfma_f32_16x16x4_f32 v[140:143], v88, v154, v[140:143]
	v_mfma_f32_16x16x4_f32 v[132:135], v88, v146, v[132:135]
	v_mfma_f32_16x16x4_f32 v[136:139], v88, v150, v[136:139]
	v_mfma_f32_16x16x4_f32 v[132:135], v89, v147, v[132:135]
	v_add_u32_e32 v216, 0x6000, v255
	global_load_dwordx4 v[144:147], v216, s[94:95]
	v_add_u32_e32 v216, 0x6100, v255
	global_load_dwordx4 v[70:73], v216, s[94:95]
	v_add_u32_e32 v216, 0x6200, v255
	global_load_dwordx4 v[74:77], v216, s[94:95]
	v_add_u32_e32 v216, 0x6c00, v255
	global_load_dwordx4 v[78:81], v216, s[94:95]
	v_mfma_f32_16x16x4_f32 v[136:139], v89, v151, v[136:139]
	v_add_u32_e32 v216, 0x6d00, v255
	global_load_dwordx4 v[148:151], v216, s[94:95]
	v_add_u32_e32 v216, 0x6e00, v255
	global_load_dwordx4 v[82:85], v216, s[94:95]
	v_add_u32_e32 v216, 0x7800, v255
	global_load_dwordx4 v[94:97], v216, s[94:95]
	v_add_u32_e32 v216, 0x7900, v255
	global_load_dwordx4 v[234:237], v216, s[94:95]
	v_add_u32_e32 v216, 0x7a00, v255
	global_load_dwordx4 v[238:241], v216, s[94:95]
	v_add_u32_e32 v216, 0x8400, v255
	global_load_dwordx4 v[242:245], v216, s[94:95]
	v_add_u32_e32 v216, 0x8500, v255
	global_load_dwordx4 v[246:249], v216, s[94:95]
	v_add_u32_e32 v216, 0x8600, v255
	global_load_dwordx4 v[250:253], v216, s[94:95]
	v_mfma_f32_16x16x4_f32 v[140:143], v89, v155, v[140:143]
	ds_read_b128 v[152:155], v123 offset:256
	ds_read_b128 v[86:89], v123 offset:320
	s_waitcnt vmcnt(23) lgkmcnt(1)
	v_mfma_f32_16x16x4_f32 v[132:135], v152, v156, v[132:135]
	s_waitcnt vmcnt(22)
	v_mfma_f32_16x16x4_f32 v[136:139], v152, v160, v[136:139]
	s_waitcnt vmcnt(21)
	v_mfma_f32_16x16x4_f32 v[140:143], v152, v164, v[140:143]
	v_mfma_f32_16x16x4_f32 v[132:135], v153, v157, v[132:135]
	v_mfma_f32_16x16x4_f32 v[136:139], v153, v161, v[136:139]
	v_mfma_f32_16x16x4_f32 v[140:143], v153, v165, v[140:143]
	v_mfma_f32_16x16x4_f32 v[132:135], v154, v158, v[132:135]
	v_mfma_f32_16x16x4_f32 v[136:139], v154, v162, v[136:139]
	v_mfma_f32_16x16x4_f32 v[140:143], v154, v166, v[140:143]
	v_mfma_f32_16x16x4_f32 v[132:135], v155, v159, v[132:135]
	v_mfma_f32_16x16x4_f32 v[136:139], v155, v163, v[136:139]
	v_mfma_f32_16x16x4_f32 v[140:143], v155, v167, v[140:143]
	ds_read_b128 v[152:155], v123 offset:384
	ds_read_b128 v[156:159], v123 offset:448
	s_waitcnt vmcnt(20) lgkmcnt(2)
	v_mfma_f32_16x16x4_f32 v[132:135], v86, v168, v[132:135]
	s_waitcnt vmcnt(19)
	v_mfma_f32_16x16x4_f32 v[136:139], v86, v172, v[136:139]
	s_waitcnt vmcnt(18)
	v_mfma_f32_16x16x4_f32 v[140:143], v86, v176, v[140:143]
	v_mfma_f32_16x16x4_f32 v[132:135], v87, v169, v[132:135]
	v_mfma_f32_16x16x4_f32 v[136:139], v87, v173, v[136:139]
	v_mfma_f32_16x16x4_f32 v[140:143], v87, v177, v[140:143]
	v_mfma_f32_16x16x4_f32 v[132:135], v88, v170, v[132:135]
	v_mfma_f32_16x16x4_f32 v[136:139], v88, v174, v[136:139]
	v_mfma_f32_16x16x4_f32 v[140:143], v88, v178, v[140:143]
	v_mfma_f32_16x16x4_f32 v[132:135], v89, v171, v[132:135]
	v_mfma_f32_16x16x4_f32 v[136:139], v89, v175, v[136:139]
	v_mfma_f32_16x16x4_f32 v[140:143], v89, v179, v[140:143]
	s_waitcnt vmcnt(17) lgkmcnt(1)
	v_mfma_f32_16x16x4_f32 v[132:135], v152, v180, v[132:135]
	s_waitcnt vmcnt(16)
	v_mfma_f32_16x16x4_f32 v[136:139], v152, v184, v[136:139]
	s_waitcnt vmcnt(15)
	v_mfma_f32_16x16x4_f32 v[140:143], v152, v188, v[140:143]
	v_mfma_f32_16x16x4_f32 v[132:135], v153, v181, v[132:135]
	v_mfma_f32_16x16x4_f32 v[136:139], v153, v185, v[136:139]
	v_mfma_f32_16x16x4_f32 v[140:143], v153, v189, v[140:143]
	v_mfma_f32_16x16x4_f32 v[132:135], v154, v182, v[132:135]
	v_mfma_f32_16x16x4_f32 v[136:139], v154, v186, v[136:139]
	v_mfma_f32_16x16x4_f32 v[140:143], v154, v190, v[140:143]
	v_mfma_f32_16x16x4_f32 v[132:135], v155, v183, v[132:135]
	v_mfma_f32_16x16x4_f32 v[136:139], v155, v187, v[136:139]
	v_mfma_f32_16x16x4_f32 v[140:143], v155, v191, v[140:143]
	v_add_u32_e32 v216, 0x9000, v255
	global_load_dwordx4 v[152:155], v216, s[94:95]
	v_add_u32_e32 v216, 0x9100, v255
	global_load_dwordx4 v[160:163], v216, s[94:95]
	v_add_u32_e32 v216, 0x9200, v255
	global_load_dwordx4 v[164:167], v216, s[94:95]
	v_add_u32_e32 v216, 0x9c00, v255
	global_load_dwordx4 v[86:89], v216, s[94:95]
	s_waitcnt vmcnt(16) lgkmcnt(0)
	v_mfma_f32_16x16x4_f32 v[140:143], v156, v230, v[140:143]
	v_mfma_f32_16x16x4_f32 v[132:135], v156, v192, v[132:135]
	v_mfma_f32_16x16x4_f32 v[136:139], v156, v226, v[136:139]
	v_mfma_f32_16x16x4_f32 v[140:143], v157, v231, v[140:143]
	v_mfma_f32_16x16x4_f32 v[132:135], v157, v193, v[132:135]
	v_mfma_f32_16x16x4_f32 v[136:139], v157, v227, v[136:139]
	v_mfma_f32_16x16x4_f32 v[140:143], v158, v232, v[140:143]
	v_mfma_f32_16x16x4_f32 v[132:135], v158, v194, v[132:135]
	v_mfma_f32_16x16x4_f32 v[136:139], v158, v228, v[136:139]
	v_mfma_f32_16x16x4_f32 v[132:135], v159, v195, v[132:135]
	v_mfma_f32_16x16x4_f32 v[136:139], v159, v229, v[136:139]
	v_add_u32_e32 v216, 0x9d00, v255
	global_load_dwordx4 v[168:171], v216, s[94:95]
	v_add_u32_e32 v216, 0x9e00, v255
	global_load_dwordx4 v[172:175], v216, s[94:95]
	v_add_u32_e32 v216, 0xa800, v255
	global_load_dwordx4 v[176:179], v216, s[94:95]
	v_add_u32_e32 v216, 0xa900, v255
	global_load_dwordx4 v[180:183], v216, s[94:95]
	v_add_u32_e32 v216, 0xaa00, v255
	global_load_dwordx4 v[184:187], v216, s[94:95]
	v_add_u32_e32 v216, 0xb400, v255
	global_load_dwordx4 v[188:191], v216, s[94:95]
	v_add_u32_e32 v216, 0xb500, v255
	global_load_dwordx4 v[192:195], v216, s[94:95]
	v_add_u32_e32 v216, 0xb600, v255
	global_load_dwordx4 v[226:229], v216, s[94:95]
	s_add_i32 s82, s68, 1
	s_min_u32 s82, s82, 3
	s_lshl_b32 s82, s82, 4
	s_add_i32 s82, s67, s82
	s_ashr_i32 s83, s82, 31
	s_lshl_b64 s[82:83], s[82:83], 13
	v_lshl_add_u64 v[98:99], v[128:129], 0, s[82:83]
	s_add_u32 s82, s82, 0x1000
	s_addc_u32 s83, s83, 0
	global_load_dwordx4 v[118:121], v[98:99], off
	global_load_dwordx4 v[114:117], v[98:99], off offset:16
	global_load_dwordx4 v[110:113], v[98:99], off offset:2048
	global_load_dwordx4 v[106:109], v[98:99], off offset:2064
	v_lshl_add_u64 v[100:101], v[128:129], 0, s[82:83]
	s_add_u32 s82, s82, 0x1000
	s_addc_u32 s83, s83, 0
	global_load_dwordx4 v[58:61], v[100:101], off offset:2064
	global_load_dwordx4 v[90:93], v[100:101], off
	global_load_dwordx4 v[66:69], v[100:101], off offset:16
	global_load_dwordx4 v[62:65], v[100:101], off offset:2048
	v_lshl_add_u64 v[98:99], v[128:129], 0, s[82:83]
	s_nop 0
	global_load_dwordx4 v[54:57], v[98:99], off
	global_load_dwordx4 v[50:53], v[98:99], off offset:16
	global_load_dwordx4 v[196:199], v[98:99], off offset:2064
	global_load_dwordx4 v[200:203], v[98:99], off offset:2048
	s_add_u32 s82, s82, 0x1000
	s_addc_u32 s83, s83, 0
	v_lshl_add_u64 v[100:101], v[128:129], 0, s[82:83]
	s_nop 0
	global_load_dwordx4 v[204:207], v[100:101], off
	global_load_dwordx4 v[208:211], v[100:101], off offset:16
	global_load_dwordx4 v[102:105], v[100:101], off offset:2048
	global_load_dwordx4 v[212:215], v[100:101], off offset:2064
	v_mfma_f32_16x16x4_f32 v[140:143], v159, v233, v[140:143]
	ds_read_b128 v[156:159], v123 offset:512
	ds_read_b128 v[230:233], v123 offset:576
	s_waitcnt vmcnt(39) lgkmcnt(1)
	v_mfma_f32_16x16x4_f32 v[132:135], v156, v144, v[132:135]
	s_waitcnt vmcnt(38)
	v_mfma_f32_16x16x4_f32 v[136:139], v156, v70, v[136:139]
	s_waitcnt vmcnt(37)
	v_mfma_f32_16x16x4_f32 v[140:143], v156, v74, v[140:143]
	v_mfma_f32_16x16x4_f32 v[132:135], v157, v145, v[132:135]
	v_mfma_f32_16x16x4_f32 v[136:139], v157, v71, v[136:139]
	v_mfma_f32_16x16x4_f32 v[140:143], v157, v75, v[140:143]
	v_mfma_f32_16x16x4_f32 v[132:135], v158, v146, v[132:135]
	v_mfma_f32_16x16x4_f32 v[136:139], v158, v72, v[136:139]
	v_mfma_f32_16x16x4_f32 v[140:143], v158, v76, v[140:143]
	v_mfma_f32_16x16x4_f32 v[132:135], v159, v147, v[132:135]
	v_mfma_f32_16x16x4_f32 v[136:139], v159, v73, v[136:139]
	v_mfma_f32_16x16x4_f32 v[140:143], v159, v77, v[140:143]
	s_waitcnt vmcnt(36) lgkmcnt(0)
	v_mfma_f32_16x16x4_f32 v[132:135], v230, v78, v[132:135]
	s_waitcnt vmcnt(35)
	v_mfma_f32_16x16x4_f32 v[136:139], v230, v148, v[136:139]
	s_waitcnt vmcnt(34)
	v_mfma_f32_16x16x4_f32 v[140:143], v230, v82, v[140:143]
	v_mfma_f32_16x16x4_f32 v[132:135], v231, v79, v[132:135]
	v_mfma_f32_16x16x4_f32 v[136:139], v231, v149, v[136:139]
	v_mfma_f32_16x16x4_f32 v[140:143], v231, v83, v[140:143]
	v_mfma_f32_16x16x4_f32 v[132:135], v232, v80, v[132:135]
	v_mfma_f32_16x16x4_f32 v[136:139], v232, v150, v[136:139]
	v_mfma_f32_16x16x4_f32 v[140:143], v232, v84, v[140:143]
	v_mfma_f32_16x16x4_f32 v[132:135], v233, v81, v[132:135]
	v_mfma_f32_16x16x4_f32 v[136:139], v233, v151, v[136:139]
	ds_read_b128 v[144:147], v123 offset:640
	ds_read_b128 v[148:151], v123 offset:704
	v_mfma_f32_16x16x4_f32 v[140:143], v233, v85, v[140:143]
	s_waitcnt vmcnt(33) lgkmcnt(1)
	v_mfma_f32_16x16x4_f32 v[132:135], v144, v94, v[132:135]
	s_waitcnt vmcnt(32)
	v_mfma_f32_16x16x4_f32 v[136:139], v144, v234, v[136:139]
	s_waitcnt vmcnt(31)
	v_mfma_f32_16x16x4_f32 v[140:143], v144, v238, v[140:143]
	v_mfma_f32_16x16x4_f32 v[132:135], v145, v95, v[132:135]
	v_mfma_f32_16x16x4_f32 v[136:139], v145, v235, v[136:139]
	v_mfma_f32_16x16x4_f32 v[140:143], v145, v239, v[140:143]
	v_mfma_f32_16x16x4_f32 v[132:135], v146, v96, v[132:135]
	v_mfma_f32_16x16x4_f32 v[136:139], v146, v236, v[136:139]
	v_mfma_f32_16x16x4_f32 v[140:143], v146, v240, v[140:143]
	v_mfma_f32_16x16x4_f32 v[132:135], v147, v97, v[132:135]
	v_mfma_f32_16x16x4_f32 v[136:139], v147, v237, v[136:139]
	v_mfma_f32_16x16x4_f32 v[140:143], v147, v241, v[140:143]
	s_waitcnt vmcnt(30) lgkmcnt(0)
	v_mfma_f32_16x16x4_f32 v[132:135], v148, v242, v[132:135]
	s_waitcnt vmcnt(29)
	v_mfma_f32_16x16x4_f32 v[136:139], v148, v246, v[136:139]
	s_waitcnt vmcnt(28)
	v_mfma_f32_16x16x4_f32 v[140:143], v148, v250, v[140:143]
	v_mfma_f32_16x16x4_f32 v[132:135], v149, v243, v[132:135]
	v_mfma_f32_16x16x4_f32 v[136:139], v149, v247, v[136:139]
	v_mfma_f32_16x16x4_f32 v[140:143], v149, v251, v[140:143]
	v_mfma_f32_16x16x4_f32 v[132:135], v150, v244, v[132:135]
	v_mfma_f32_16x16x4_f32 v[136:139], v150, v248, v[136:139]
	v_mfma_f32_16x16x4_f32 v[140:143], v150, v252, v[140:143]
	v_mfma_f32_16x16x4_f32 v[132:135], v151, v245, v[132:135]
	v_mfma_f32_16x16x4_f32 v[136:139], v151, v249, v[136:139]
	v_mfma_f32_16x16x4_f32 v[140:143], v151, v253, v[140:143]
	ds_read_b128 v[144:147], v123 offset:768
	ds_read_b128 v[148:151], v123 offset:832
	s_waitcnt vmcnt(27) lgkmcnt(1)
	v_mfma_f32_16x16x4_f32 v[132:135], v144, v152, v[132:135]
	s_waitcnt vmcnt(26)
	v_mfma_f32_16x16x4_f32 v[136:139], v144, v160, v[136:139]
	s_waitcnt vmcnt(25)
	v_mfma_f32_16x16x4_f32 v[140:143], v144, v164, v[140:143]
	v_mfma_f32_16x16x4_f32 v[132:135], v145, v153, v[132:135]
	v_mfma_f32_16x16x4_f32 v[136:139], v145, v161, v[136:139]
	v_mfma_f32_16x16x4_f32 v[140:143], v145, v165, v[140:143]
	v_mfma_f32_16x16x4_f32 v[132:135], v146, v154, v[132:135]
	v_mfma_f32_16x16x4_f32 v[136:139], v146, v162, v[136:139]
	v_mfma_f32_16x16x4_f32 v[140:143], v146, v166, v[140:143]
	v_mfma_f32_16x16x4_f32 v[132:135], v147, v155, v[132:135]
	v_mfma_f32_16x16x4_f32 v[136:139], v147, v163, v[136:139]
	v_mfma_f32_16x16x4_f32 v[140:143], v147, v167, v[140:143]
	s_waitcnt vmcnt(24) lgkmcnt(0)
	v_mfma_f32_16x16x4_f32 v[132:135], v148, v86, v[132:135]
	s_waitcnt vmcnt(23)
	v_mfma_f32_16x16x4_f32 v[136:139], v148, v168, v[136:139]
	s_waitcnt vmcnt(22)
	v_mfma_f32_16x16x4_f32 v[140:143], v148, v172, v[140:143]
	v_mfma_f32_16x16x4_f32 v[132:135], v149, v87, v[132:135]
	v_mfma_f32_16x16x4_f32 v[136:139], v149, v169, v[136:139]
	v_mfma_f32_16x16x4_f32 v[140:143], v149, v173, v[140:143]
	v_mfma_f32_16x16x4_f32 v[132:135], v150, v88, v[132:135]
	v_mfma_f32_16x16x4_f32 v[136:139], v150, v170, v[136:139]
	v_mfma_f32_16x16x4_f32 v[140:143], v150, v174, v[140:143]
	v_mfma_f32_16x16x4_f32 v[132:135], v151, v89, v[132:135]
	v_mfma_f32_16x16x4_f32 v[136:139], v151, v171, v[136:139]
	v_mfma_f32_16x16x4_f32 v[140:143], v151, v175, v[140:143]
	ds_read_b128 v[144:147], v123 offset:896
	ds_read_b128 v[148:151], v123 offset:960
	s_waitcnt vmcnt(21) lgkmcnt(1)
	v_mfma_f32_16x16x4_f32 v[132:135], v144, v176, v[132:135]
	s_waitcnt vmcnt(20)
	v_mfma_f32_16x16x4_f32 v[136:139], v144, v180, v[136:139]
	s_waitcnt vmcnt(19)
	v_mfma_f32_16x16x4_f32 v[140:143], v144, v184, v[140:143]
	v_mfma_f32_16x16x4_f32 v[132:135], v145, v177, v[132:135]
	v_mfma_f32_16x16x4_f32 v[136:139], v145, v181, v[136:139]
	v_mfma_f32_16x16x4_f32 v[140:143], v145, v185, v[140:143]
	v_mfma_f32_16x16x4_f32 v[132:135], v146, v178, v[132:135]
	v_mfma_f32_16x16x4_f32 v[136:139], v146, v182, v[136:139]
	v_mfma_f32_16x16x4_f32 v[140:143], v146, v186, v[140:143]
	v_mfma_f32_16x16x4_f32 v[132:135], v147, v179, v[132:135]
	v_mfma_f32_16x16x4_f32 v[136:139], v147, v183, v[136:139]
	v_mfma_f32_16x16x4_f32 v[140:143], v147, v187, v[140:143]
	s_waitcnt vmcnt(18) lgkmcnt(0)
	v_mfma_f32_16x16x4_f32 v[132:135], v148, v188, v[132:135]
	s_waitcnt vmcnt(17)
	v_mfma_f32_16x16x4_f32 v[136:139], v148, v192, v[136:139]
	s_waitcnt vmcnt(16)
	v_mfma_f32_16x16x4_f32 v[140:143], v148, v226, v[140:143]
	v_mfma_f32_16x16x4_f32 v[132:135], v149, v189, v[132:135]
	v_mfma_f32_16x16x4_f32 v[136:139], v149, v193, v[136:139]
	v_mfma_f32_16x16x4_f32 v[140:143], v149, v227, v[140:143]
	v_mfma_f32_16x16x4_f32 v[132:135], v150, v190, v[132:135]
	v_mfma_f32_16x16x4_f32 v[136:139], v150, v194, v[136:139]
	v_mfma_f32_16x16x4_f32 v[140:143], v150, v228, v[140:143]
	v_mfma_f32_16x16x4_f32 v[132:135], v151, v191, v[132:135]
	v_mfma_f32_16x16x4_f32 v[136:139], v151, v195, v[136:139]
	v_mfma_f32_16x16x4_f32 v[140:143], v151, v229, v[140:143]
	s_nop 8
	ds_write2_b32 v223, v132, v136 offset1:16
	ds_write2_b32 v223, v140, v133 offset0:32 offset1:48
	ds_write2_b32 v223, v137, v141 offset0:64 offset1:80
	ds_write2_b32 v223, v134, v138 offset0:96 offset1:112
	ds_write2_b32 v223, v142, v135 offset0:128 offset1:144
	ds_write2_b32 v223, v139, v143 offset0:160 offset1:176
	s_waitcnt lgkmcnt(0)
	s_barrier
	s_and_saveexec_b64 s[6:7], s[4:5]
	s_cbranch_execz .LBB0_595
	s_mov_b64 s[8:9], 0
	v_mov_b32_e32 v34, v0

.LBB0_1294:
	s_cmp_lt_i32 s30, 14
	s_cselect_b64 s[2:3], -1, 0
	s_and_b64 s[40:41], s[2:3], s[0:1]
	s_andn2_b64 vcc, exec, s[40:41]
	s_cbranch_vccnz .LBB0_1318
	s_cmpk_gt_i32 s93, 0xff
	s_cbranch_scc1 .LBB0_1318
	v_and_b32_e32 v7, 63, v0
	v_mov_b32_e32 v125, 0
	v_readlane_b32 s0, v254, 12
	v_lshlrev_b32_e32 v122, 5, v7
	v_mov_b32_e32 v123, v125
	v_readlane_b32 s1, v254, 13
	v_readlane_b32 s14, v254, 26
	v_readlane_b32 s15, v254, 27
	s_mov_b64 s[0:1], 0x2000
	v_readlane_b32 s6, v254, 18
	v_lshl_add_u64 v[2:3], s[14:15], 0, v[122:123]
	s_waitcnt vmcnt(0)
	v_lshl_add_u64 v[34:35], v[2:3], 0, s[0:1]
	s_mov_b64 s[0:1], 0x3000
	v_lshl_add_u64 v[36:37], v[2:3], 0, s[0:1]
	s_mov_b64 s[0:1], 0x3800
	v_lshl_add_u64 v[38:39], v[2:3], 0, s[0:1]
	v_readlane_b32 s0, v254, 0
	v_readlane_b32 s2, v254, 14
	s_andn2_b32 s0, s0, 63
	v_lshrrev_b32_e32 v1, 4, v7
	v_readlane_b32 s6, v254, 8
	v_readlane_b32 s4, v254, 16
	v_or_b32_e32 v4, s0, v1
	s_lshl_b32 s2, s6, 1
	v_mad_i64_i32 v[4:5], s[0:1], v4, 48, 0
	v_and_b32_e32 v6, 15, v0
	s_mul_i32 s4, s6, 0x4020
	s_or_b32 s33, s2, 1
	v_readlane_b32 s5, v254, 17
	v_or_b32_e32 v4, v4, v6
	s_add_i32 s26, s4, 0
	s_mul_i32 s4, s33, 0x2010
	v_lshl_add_u64 v[40:41], v[4:5], 4, s[28:29]
	s_add_i32 s34, s4, 0
	s_mov_b64 s[4:5], 0x4eb61800
	v_lshl_add_u64 v[132:133], v[40:41], 0, s[4:5]
	s_mov_b64 s[4:5], 0x4eb61900
	v_lshl_add_u64 v[134:135], v[40:41], 0, s[4:5]
	s_mov_b64 s[4:5], 0x4eb61a00
	v_lshl_add_u64 v[136:137], v[40:41], 0, s[4:5]
	s_mov_b64 s[4:5], 0x4eb62400
	v_lshl_add_u64 v[138:139], v[40:41], 0, s[4:5]
	s_mov_b64 s[4:5], 0x4eb62500
	v_lshl_add_u64 v[140:141], v[40:41], 0, s[4:5]
	s_mov_b64 s[4:5], 0x4eb62600
	v_lshl_add_u64 v[142:143], v[40:41], 0, s[4:5]
	s_mov_b64 s[4:5], 0x4eb63000
	v_lshl_add_u64 v[144:145], v[40:41], 0, s[4:5]
	s_mov_b64 s[4:5], 0x4eb63100
	v_lshl_add_u64 v[146:147], v[40:41], 0, s[4:5]
	s_mov_b64 s[4:5], 0x4eb63200
	v_lshl_add_u64 v[148:149], v[40:41], 0, s[4:5]
	s_mov_b64 s[4:5], 0x4eb63c00
	v_lshl_add_u64 v[150:151], v[40:41], 0, s[4:5]
	s_mov_b64 s[4:5], 0x4eb63d00
	v_lshl_add_u64 v[152:153], v[40:41], 0, s[4:5]
	s_mov_b64 s[4:5], 0x4eb63e00
	v_lshl_add_u64 v[154:155], v[40:41], 0, s[4:5]
	s_mov_b64 s[4:5], 0x4eb64800
	v_lshl_add_u64 v[156:157], v[40:41], 0, s[4:5]
	s_mov_b64 s[4:5], 0x4eb64900
	v_lshl_add_u64 v[158:159], v[40:41], 0, s[4:5]
	s_mov_b64 s[4:5], 0x4eb64a00
	v_lshl_add_u64 v[160:161], v[40:41], 0, s[4:5]
	s_mov_b64 s[4:5], 0x4eb65400
	v_lshl_add_u64 v[162:163], v[40:41], 0, s[4:5]
	s_mov_b64 s[4:5], 0x4eb65500
	v_lshl_add_u64 v[164:165], v[40:41], 0, s[4:5]
	s_mov_b64 s[4:5], 0x4eb65600
	v_lshl_add_u64 v[166:167], v[40:41], 0, s[4:5]
	s_mov_b64 s[4:5], 0x4eb66000
	v_lshl_add_u64 v[168:169], v[40:41], 0, s[4:5]
	s_mov_b64 s[4:5], 0x4eb66100
	v_lshl_add_u64 v[170:171], v[40:41], 0, s[4:5]
	s_mov_b64 s[4:5], 0x4eb66200
	v_lshl_add_u64 v[172:173], v[40:41], 0, s[4:5]
	s_mov_b64 s[4:5], 0x4eb66c00
	v_lshl_add_u64 v[174:175], v[40:41], 0, s[4:5]
	s_mov_b64 s[4:5], 0x4eb66d00
	v_lshl_add_u64 v[176:177], v[40:41], 0, s[4:5]
	s_mov_b64 s[4:5], 0x4eb66e00
	s_mov_b64 s[0:1], 0x4eb60000
	v_lshl_add_u64 v[178:179], v[40:41], 0, s[4:5]
	s_mov_b64 s[4:5], 0x4eb67800
	v_readlane_b32 s3, v254, 15
	v_lshl_add_u64 v[126:127], v[40:41], 0, s[0:1]
	s_nop 3
	v_readfirstlane_b32 s94, v126
	v_readfirstlane_b32 s95, v127
	s_nop 3
	v_subrev_u32_e32 v255, s94, v126
	s_lshl_b32 s0, s6, 10
	v_lshl_add_u64 v[180:181], v[40:41], 0, s[4:5]
	s_movk_i32 s4, 0x3000
	v_mul_u32_u24_e32 v4, 0x2010, v6
	s_add_i32 s0, s0, 0
	v_and_b32_e32 v5, 48, v7
	s_add_i32 s3, 0, 0x20100
	v_add_co_u32_e32 v42, vcc, s4, v2
	v_lshl_add_u64 v[128:129], s[50:51], 0, v[122:123]
	v_lshlrev_b32_e32 v124, 4, v7
	v_add3_u32 v123, s0, v4, v5
	v_lshl_add_u32 v44, v6, 2, s3
	v_cmp_eq_u32_e64 s[0:1], 0, v7
	v_addc_co_u32_e32 v43, vcc, 0, v3, vcc
	global_load_dwordx4 v[2:5], v[34:35], off offset:16
	global_load_dwordx4 v[6:9], v[34:35], off offset:2048
	global_load_dwordx4 v[10:13], v[34:35], off offset:2064
	global_load_dwordx4 v[14:17], v[36:37], off offset:16
	global_load_dwordx4 v[18:21], v[42:43], off
	global_load_dwordx4 v[22:25], v[42:43], off offset:2048
	global_load_dwordx4 v[26:29], v[42:43], off offset:-4096
	global_load_dwordx4 v[30:33], v[38:39], off offset:16
	s_mov_b64 s[4:5], 0x4eb67900
	v_lshl_add_u64 v[182:183], v[40:41], 0, s[4:5]
	s_mov_b64 s[4:5], 0x4eb67a00
	v_lshl_add_u64 v[184:185], v[40:41], 0, s[4:5]
	s_mov_b64 s[4:5], 0x4eb68400
	v_lshl_add_u64 v[186:187], v[40:41], 0, s[4:5]
	s_mov_b64 s[4:5], 0x4eb68500
	v_lshl_add_u64 v[188:189], v[40:41], 0, s[4:5]
	s_mov_b64 s[4:5], 0x4eb68600
	v_lshl_add_u64 v[190:191], v[40:41], 0, s[4:5]
	s_mov_b64 s[4:5], 0x4eb69000
	v_lshl_add_u64 v[192:193], v[40:41], 0, s[4:5]
	s_mov_b64 s[4:5], 0x4eb69100
	v_lshl_add_u64 v[194:195], v[40:41], 0, s[4:5]
	s_mov_b64 s[4:5], 0x4eb69200
	v_lshl_add_u64 v[196:197], v[40:41], 0, s[4:5]
	s_mov_b64 s[4:5], 0x4eb69c00
	v_lshl_add_u64 v[198:199], v[40:41], 0, s[4:5]
	s_mov_b64 s[4:5], 0x4eb69d00
	v_lshl_add_u64 v[200:201], v[40:41], 0, s[4:5]
	s_mov_b64 s[4:5], 0x4eb69e00
	v_lshl_add_u64 v[202:203], v[40:41], 0, s[4:5]
	s_mov_b64 s[4:5], 0x4eb6a800
	v_lshl_add_u64 v[204:205], v[40:41], 0, s[4:5]
	s_mov_b64 s[4:5], 0x4eb6a900
	v_lshl_add_u64 v[206:207], v[40:41], 0, s[4:5]
	s_mov_b64 s[4:5], 0x4eb6aa00
	v_lshl_add_u64 v[208:209], v[40:41], 0, s[4:5]
	s_mov_b64 s[4:5], 0x4eb6b400
	v_lshl_add_u64 v[210:211], v[40:41], 0, s[4:5]
	s_mov_b64 s[4:5], 0x4eb6b500
	v_lshlrev_b32_e32 v1, 2, v1
	v_lshl_add_u64 v[212:213], v[40:41], 0, s[4:5]
	s_mov_b64 s[4:5], 0x4eb6b600
	v_lshl_or_b32 v1, s6, 4, v1
	v_lshl_add_u64 v[214:215], v[40:41], 0, s[4:5]
	s_movk_i32 s4, 0xc0
	v_mul_lo_u32 v1, v1, s4
	s_mul_i32 s4, s6, 0x140
	s_add_i32 s35, 0, 0x26100
	s_add_i32 s68, s35, s4
	s_mul_i32 s4, s33, 0xa0
	v_readlane_b32 s10, v254, 22
	v_readlane_b32 s11, v254, 23
	s_add_i32 s69, s35, s4
	s_movk_i32 s4, 0x240
	s_add_i32 s6, 0, 0x26b00
	v_mbcnt_lo_u32_b32 v34, -1, 0
	v_lshl_add_u64 v[130:131], s[36:37], 0, v[124:125]
	v_cmp_gt_u32_e64 s[10:11], 32, v0
	v_cmp_gt_u32_e64 s[4:5], s4, v0
	v_lshl_add_u32 v218, v0, 2, s6
	s_mov_b64 s[54:55], 0x1000
	s_movk_i32 s70, 0x1000
	s_mov_b64 s[56:57], 0x1800
	v_mbcnt_hi_u32_b32 v220, -1, v34
	v_mov_b32_e32 v221, 0x358637bd
	s_mov_b32 s71, 0xf800000
	v_mov_b32_e32 v222, 0x260
	v_add_u32_e32 v223, v44, v1
	s_mov_b32 s72, 0xe38f
	s_mov_b64 s[58:59], 0x70
	s_mov_b32 s73, 0xff61b1e6
	v_mov_b32_e32 v224, 0xff61b1e6
	v_readlane_b32 s7, v254, 19
	v_readlane_b32 s8, v254, 20
	v_readlane_b32 s9, v254, 21
	v_readlane_b32 s12, v254, 24
	v_readlane_b32 s13, v254, 25
	v_mov_b32_e32 v40, v0
	v_mov_b32_e32 v45, 0
	v_mul_u32_u24_sdwa v41, v40, s72 dst_sel:DWORD dst_unused:UNUSED_PAD src0_sel:WORD_0 src1_sel:DWORD
	v_lshrrev_b32_e32 v41, 21, v41
	v_mul_lo_u16_e32 v42, 36, v41
	v_sub_u16_e32 v42, v40, v42
	v_lshlrev_b32_e32 v44, 2, v42
	v_lshl_add_u64 v[36:37], s[38:39], 0, v[44:45]
	v_lshl_add_u64 v[38:39], s[42:43], 0, v[44:45]
	v_lshl_add_u64 v[36:37], v[36:37], 0, 16
	v_lshl_add_u64 v[38:39], v[38:39], 0, s[58:59]
	v_cmp_gt_u16_e32 vcc, 4, v42
	s_nop 1
	v_cndmask_b32_e32 v37, v39, v37, vcc
	v_cndmask_b32_e32 v36, v38, v36, vcc
	global_load_dword v42, v[36:37], off
	v_lshlrev_b32_e32 v43, 2, v40
	v_add_u32_e32 v43, 0x26c00, v43
	s_waitcnt vmcnt(0)
	ds_write_b32 v43, v42
	v_add_u32_e32 v40, 0x200, v40
	v_cmp_gt_u32_e32 vcc, 0x240, v40
	s_and_saveexec_b64 s[14:15], vcc
	v_mul_u32_u24_sdwa v41, v40, s72 dst_sel:DWORD dst_unused:UNUSED_PAD src0_sel:WORD_0 src1_sel:DWORD
	v_lshrrev_b32_e32 v41, 21, v41
	v_mul_lo_u16_e32 v42, 36, v41
	v_sub_u16_e32 v42, v40, v42
	v_lshlrev_b32_e32 v44, 2, v42
	v_lshl_add_u64 v[36:37], s[38:39], 0, v[44:45]
	v_lshl_add_u64 v[38:39], s[42:43], 0, v[44:45]
	v_lshl_add_u64 v[36:37], v[36:37], 0, 16
	v_lshl_add_u64 v[38:39], v[38:39], 0, s[58:59]
	v_cmp_gt_u16_e32 vcc, 4, v42
	s_nop 1
	v_cndmask_b32_e32 v37, v39, v37, vcc
	v_cndmask_b32_e32 v36, v38, v36, vcc
	global_load_dword v42, v[36:37], off
	v_lshlrev_b32_e32 v43, 2, v40
	v_add_u32_e32 v43, 0x26c00, v43
	s_waitcnt vmcnt(0)
	ds_write_b32 v43, v42
	s_or_b64 exec, exec, s[14:15]
	s_branch .LBB0_1298

.LBB0_1298:
	s_and_saveexec_b64 s[6:7], s[10:11]
	ds_write_b32 v218, v125
	s_or_b64 exec, exec, s[6:7]
	s_lshl_b32 s75, s93, 6
	s_add_i32 s76, s75, s2
	s_mov_b32 s77, 0
	s_waitcnt lgkmcnt(0)
	s_barrier
	s_mov_b32 s82, 0
	s_lshl_b32 s82, s82, 4
	s_add_i32 s82, s76, s82
	s_ashr_i32 s83, s82, 31
	s_lshl_b64 s[82:83], s[82:83], 13
	v_lshl_add_u64 v[98:99], v[128:129], 0, s[82:83]
	s_add_u32 s82, s82, 0x1000
	s_addc_u32 s83, s83, 0
	global_load_dwordx4 v[118:121], v[98:99], off
	global_load_dwordx4 v[114:117], v[98:99], off offset:16
	global_load_dwordx4 v[110:113], v[98:99], off offset:2048
	global_load_dwordx4 v[106:109], v[98:99], off offset:2064
	v_lshl_add_u64 v[100:101], v[128:129], 0, s[82:83]
	s_add_u32 s82, s82, 0x1000
	s_addc_u32 s83, s83, 0
	global_load_dwordx4 v[58:61], v[100:101], off offset:2064
	global_load_dwordx4 v[90:93], v[100:101], off
	global_load_dwordx4 v[66:69], v[100:101], off offset:16
	global_load_dwordx4 v[62:65], v[100:101], off offset:2048
	v_lshl_add_u64 v[98:99], v[128:129], 0, s[82:83]
	s_nop 0
	global_load_dwordx4 v[54:57], v[98:99], off
	global_load_dwordx4 v[50:53], v[98:99], off offset:16
	global_load_dwordx4 v[196:199], v[98:99], off offset:2064
	global_load_dwordx4 v[200:203], v[98:99], off offset:2048
	s_add_u32 s82, s82, 0x1000
	s_addc_u32 s83, s83, 0
	v_lshl_add_u64 v[100:101], v[128:129], 0, s[82:83]
	s_nop 0
	global_load_dwordx4 v[204:207], v[100:101], off
	global_load_dwordx4 v[208:211], v[100:101], off offset:16
	global_load_dwordx4 v[102:105], v[100:101], off offset:2048
	global_load_dwordx4 v[212:215], v[100:101], off offset:2064
	s_branch .LBB0_1303

.LBB0_1303:
	s_lshl_b32 s8, s77, 4
	s_add_i32 s6, s76, s8
	s_ashr_i32 s7, s6, 31
	s_lshl_b64 s[12:13], s[6:7], 13
	v_lshl_add_u64 v[34:35], v[128:129], 0, s[12:13]
	v_lshl_add_u64 v[36:37], v[34:35], 0, s[56:57]
	v_add_co_u32_e32 v36, vcc, 0x1000, v34
	v_and_b32_e32 v1, 64, v220
	s_nop 0
	v_addc_co_u32_e32 v37, vcc, 0, v35, vcc
	v_lshl_add_u64 v[34:35], v[34:35], 0, s[54:55]
	v_xor_b32_e32 v34, 1, v220
	v_add_u32_e32 v1, 64, v1
	s_or_b32 s6, s6, 1
	v_cmp_lt_i32_e32 vcc, v34, v1
	s_ashr_i32 s7, s6, 31
	s_lshl_b64 s[6:7], s[6:7], 13
	v_cndmask_b32_e32 v34, v220, v34, vcc
	v_lshlrev_b32_e32 v225, 2, v34
	v_lshl_add_u64 v[34:35], v[128:129], 0, s[6:7]
	v_add_co_u32_e32 v70, vcc, s70, v34
	v_lshl_add_u64 v[36:37], v[34:35], 0, s[54:55]
	s_nop 0
	v_addc_co_u32_e32 v71, vcc, 0, v35, vcc
	v_lshl_add_u64 v[72:73], v[34:35], 0, s[56:57]
	s_nop 0
	s_add_i32 s8, s8, s75
	s_add_i32 s60, s8, s2
	s_ashr_i32 s61, s60, 31
	s_add_i32 s62, s8, s33
	s_ashr_i32 s63, s62, 31
	s_waitcnt vmcnt(13)
	v_mov_b32_e32 v76, v119
	s_waitcnt vmcnt(12)
	v_mov_b32_e32 v77, v115
	v_mov_b32_e32 v80, v121
	v_mov_b32_e32 v81, v117
	v_mov_b32_e32 v74, v118
	v_mov_b32_e32 v75, v114
	v_mov_b32_e32 v78, v120
	v_mov_b32_e32 v79, v116
	s_waitcnt vmcnt(11)
	v_pk_mul_f32 v[82:83], v[112:113], v[112:113]
	v_pk_mul_f32 v[84:85], v[110:111], v[110:111]
	v_pk_mul_f32 v[76:77], v[76:77], v[76:77]
	v_pk_mul_f32 v[80:81], v[80:81], v[80:81]
	v_pk_mov_b32 v[94:95], v[84:85], v[82:83] op_sel:[1,0]
	v_mov_b32_e32 v85, v83
	v_pk_fma_f32 v[74:75], v[74:75], v[74:75], v[76:77]
	v_pk_fma_f32 v[76:77], v[78:79], v[78:79], v[80:81]
	s_waitcnt vmcnt(10)
	v_mul_f32_e32 v86, v107, v107
	v_mul_f32_e32 v88, v109, v109
	v_pk_add_f32 v[78:79], v[94:95], v[84:85]
	v_pk_add_f32 v[74:75], v[74:75], v[76:77]
	v_pk_fma_f32 v[82:83], v[106:107], v[106:107], v[86:87] op_sel_hi:[1,1,0]
	v_pk_fma_f32 v[86:87], v[108:109], v[108:109], v[88:89] op_sel_hi:[1,1,0]
	s_waitcnt vmcnt(8)
	v_mul_f32_e32 v95, v90, v90
	v_mul_f32_e32 v100, v91, v91
	v_pk_add_f32 v[76:77], v[78:79], v[78:79] op_sel:[0,1] op_sel_hi:[1,0]
	v_pk_add_f32 v[74:75], v[74:75], v[74:75] op_sel:[0,1] op_sel_hi:[1,0]
	v_mul_f32_e32 v83, v92, v92
	v_mul_f32_e32 v87, v93, v93
	s_waitcnt vmcnt(7)
	v_pk_mul_f32 v[80:81], v[68:69], v[68:69]
	v_pk_mul_f32 v[84:85], v[66:67], v[66:67]
	v_mov_b32_e32 v77, v100
	v_mov_b32_e32 v75, v95
	v_pk_mov_b32 v[78:79], v[84:85], v[80:81] op_sel:[1,0]
	v_mov_b32_e32 v85, v81
	v_pk_add_f32 v[82:83], v[82:83], v[86:87]
	v_pk_add_f32 v[74:75], v[74:75], v[76:77]
	s_waitcnt vmcnt(6)
	v_mul_f32_e32 v88, v63, v63
	v_mul_f32_e32 v94, v65, v65
	v_pk_add_f32 v[78:79], v[78:79], v[84:85]
	v_pk_add_f32 v[74:75], v[74:75], v[82:83]
	v_mul_f32_e32 v96, v58, v58
	v_mul_f32_e32 v97, v59, v59
	v_mul_f32_e32 v98, v60, v60
	v_mul_f32_e32 v99, v61, v61
	v_pk_fma_f32 v[80:81], v[62:63], v[62:63], v[88:89] op_sel_hi:[1,1,0]
	v_pk_fma_f32 v[88:89], v[64:65], v[64:65], v[94:95] op_sel_hi:[1,1,0]
	v_pk_add_f32 v[78:79], v[78:79], v[78:79] op_sel:[0,1] op_sel_hi:[1,0]
	v_pk_add_f32 v[74:75], v[74:75], v[74:75] op_sel:[0,1] op_sel_hi:[1,0]
	v_mov_b32_e32 v81, v98
	v_mov_b32_e32 v79, v97
	v_mov_b32_e32 v75, v96
	v_mov_b32_e32 v89, v99
	v_pk_add_f32 v[74:75], v[74:75], v[78:79]
	v_pk_add_f32 v[76:77], v[80:81], v[88:89]
	s_waitcnt vmcnt(0)
	v_mov_b32_e32 v42, v196
	v_mov_b32_e32 v43, v197
	v_mov_b32_e32 v44, v198
	v_mov_b32_e32 v45, v199
	v_mov_b32_e32 v46, v200
	v_mov_b32_e32 v47, v201
	v_mov_b32_e32 v48, v202
	v_mov_b32_e32 v49, v203
	v_mov_b32_e32 v38, v204
	v_mov_b32_e32 v39, v205
	v_mov_b32_e32 v40, v206
	v_mov_b32_e32 v41, v207
	v_mov_b32_e32 v34, v208
	v_mov_b32_e32 v35, v209
	v_mov_b32_e32 v36, v210
	v_mov_b32_e32 v37, v211
	v_mov_b32_e32 v98, v212
	v_mov_b32_e32 v99, v213
	v_mov_b32_e32 v100, v214
	v_mov_b32_e32 v101, v215
	global_load_dwordx4 v[82:85], v[126:127], off
	global_load_dwordx4 v[86:89], v[126:127], off offset:256
	v_pk_add_f32 v[74:75], v[74:75], v[76:77]
	v_xor_b32_e32 v76, 2, v220
	v_add_f32_e32 v74, v74, v75
	ds_bpermute_b32 v75, v225, v74
	v_cmp_lt_i32_e32 vcc, v76, v1
	s_waitcnt lgkmcnt(0)
	v_add_f32_e32 v74, v74, v75
	v_cndmask_b32_e32 v76, v220, v76, vcc
	v_lshlrev_b32_e32 v230, 2, v76
	ds_bpermute_b32 v75, v230, v74
	v_xor_b32_e32 v76, 4, v220
	v_cmp_lt_i32_e32 vcc, v76, v1
	s_waitcnt lgkmcnt(0)
	v_add_f32_e32 v74, v74, v75
	v_cndmask_b32_e32 v76, v220, v76, vcc
	v_lshlrev_b32_e32 v231, 2, v76
	ds_bpermute_b32 v75, v231, v74
	v_xor_b32_e32 v76, 8, v220
	v_cmp_lt_i32_e32 vcc, v76, v1
	s_waitcnt lgkmcnt(0)
	v_add_f32_e32 v74, v74, v75
	v_cndmask_b32_e32 v76, v220, v76, vcc
	v_lshlrev_b32_e32 v232, 2, v76
	ds_bpermute_b32 v75, v232, v74
	v_xor_b32_e32 v76, 16, v220
	v_cmp_lt_i32_e32 vcc, v76, v1
	s_waitcnt lgkmcnt(0)
	v_add_f32_e32 v74, v74, v75
	v_cndmask_b32_e32 v76, v220, v76, vcc
	v_lshlrev_b32_e32 v233, 2, v76
	ds_bpermute_b32 v75, v233, v74
	v_xor_b32_e32 v76, 32, v220
	v_cmp_lt_i32_e32 vcc, v76, v1
	s_waitcnt lgkmcnt(0)
	v_add_f32_e32 v74, v74, v75
	v_cndmask_b32_e32 v1, v220, v76, vcc
	v_lshlrev_b32_e32 v1, 2, v1
	ds_bpermute_b32 v75, v1, v74
	s_waitcnt lgkmcnt(0)
	v_add_f32_e32 v70, v74, v75
	v_fmamk_f32 v70, v70, 0x3a000000, v221
	v_mul_f32_e32 v71, 0x4f800000, v70
	v_cmp_gt_f32_e32 vcc, s71, v70
	s_nop 1
	v_cndmask_b32_e32 v124, v70, v71, vcc
	v_sqrt_f32_e32 v216, v124
	global_load_dwordx4 v[94:97], v[126:127], off offset:512
	global_load_dwordx4 v[70:73], v[126:127], off offset:3072
	global_load_dwordx4 v[74:77], v[126:127], off offset:3328
	global_load_dwordx4 v[78:81], v[126:127], off offset:3584
	v_add_u32_e32 v217, -1, v216
	v_fma_f32 v226, -v217, v216, v124
	v_cmp_ge_f32_e64 s[6:7], 0, v226
	v_add_u32_e32 v226, 1, v216
	s_nop 0
	v_cndmask_b32_e64 v217, v216, v217, s[6:7]
	v_fma_f32 v216, -v226, v216, v124
	v_cmp_lt_f32_e64 s[6:7], 0, v216
	s_nop 1
	v_cndmask_b32_e64 v216, v217, v226, s[6:7]
	v_mul_f32_e32 v217, 0x37800000, v216
	v_cndmask_b32_e32 v216, v216, v217, vcc
	v_cmp_class_f32_e32 vcc, v124, v222
	s_nop 1
	v_cndmask_b32_e32 v124, v216, v124, vcc
	v_div_scale_f32 v216, s[6:7], v124, v124, 1.0
	v_rcp_f32_e32 v217, v216
	s_lshl_b64 s[6:7], s[60:61], 12
	v_fma_f32 v226, -v216, v217, 1.0
	v_fmac_f32_e32 v217, v226, v217
	v_div_scale_f32 v226, vcc, 1.0, v124, 1.0
	v_mul_f32_e32 v227, v226, v217
	v_fma_f32 v228, -v216, v227, v226
	v_fmac_f32_e32 v227, v228, v217
	v_fma_f32 v216, -v216, v227, v226
	v_div_fmas_f32 v216, v216, v217, v227
	v_div_fixup_f32 v124, v216, v124, 1.0
	v_pk_mul_f32 v[118:119], v[118:119], v[124:125] op_sel_hi:[1,0]
	v_pk_mul_f32 v[120:121], v[120:121], v[124:125] op_sel_hi:[1,0]
	v_pk_mul_f32 v[114:115], v[114:115], v[124:125] op_sel_hi:[1,0]
	v_pk_mul_f32 v[116:117], v[116:117], v[124:125] op_sel_hi:[1,0]
	v_pk_mul_f32 v[120:121], v[28:29], v[120:121]
	v_pk_mul_f32 v[118:119], v[26:27], v[118:119]
	v_pk_mul_f32 v[116:117], v[4:5], v[116:117]
	v_pk_mul_f32 v[114:115], v[2:3], v[114:115]
	v_lshl_add_u64 v[216:217], v[130:131], 0, s[6:7]
	v_cvt_pk_bf16_f32 v226, v118, v119
	v_cvt_pk_bf16_f32 v227, v120, v121
	v_cvt_pk_bf16_f32 v228, v114, v115
	v_cvt_pk_bf16_f32 v229, v116, v117
	v_pk_mul_f32 v[110:111], v[110:111], v[124:125] op_sel_hi:[1,0]
	v_pk_mul_f32 v[112:113], v[112:113], v[124:125] op_sel_hi:[1,0]
	v_pk_mul_f32 v[106:107], v[106:107], v[124:125] op_sel_hi:[1,0]
	v_pk_mul_f32 v[108:109], v[108:109], v[124:125] op_sel_hi:[1,0]
	global_store_dwordx4 v[216:217], v[226:229], off
	v_pk_mul_f32 v[112:113], v[8:9], v[112:113]
	v_pk_mul_f32 v[110:111], v[6:7], v[110:111]
	v_add_u32_e32 v226, s26, v122
	v_pk_mul_f32 v[108:109], v[12:13], v[108:109]
	v_pk_mul_f32 v[106:107], v[10:11], v[106:107]
	ds_write_b128 v226, v[118:121]
	ds_write_b128 v226, v[114:117] offset:16
	v_cvt_pk_bf16_f32 v114, v110, v111
	v_cvt_pk_bf16_f32 v115, v112, v113
	v_cvt_pk_bf16_f32 v116, v106, v107
	v_cvt_pk_bf16_f32 v117, v108, v109
	global_store_dwordx4 v[216:217], v[114:117], off offset:1024
	ds_write_b128 v226, v[110:113] offset:2048
	ds_write_b128 v226, v[106:109] offset:2064
	s_waitcnt vmcnt(15)
	v_mov_b32_e32 v108, v55
	s_waitcnt vmcnt(14)
	v_mov_b32_e32 v109, v51
	v_mov_b32_e32 v106, v54
	v_mov_b32_e32 v107, v50
	v_pk_mul_f32 v[108:109], v[108:109], v[108:109]
	v_mov_b32_e32 v110, v57
	v_mov_b32_e32 v111, v53
	v_pk_fma_f32 v[106:107], v[106:107], v[106:107], v[108:109]
	v_mov_b32_e32 v108, v56
	v_mov_b32_e32 v109, v52
	v_pk_mul_f32 v[110:111], v[110:111], v[110:111]
	v_pk_mul_f32 v[90:91], v[90:91], v[124:125] op_sel_hi:[1,0]
	v_pk_fma_f32 v[108:109], v[108:109], v[108:109], v[110:111]
	s_waitcnt vmcnt(12)
	v_pk_mul_f32 v[110:111], v[46:47], v[46:47]
	v_pk_add_f32 v[106:107], v[106:107], v[108:109]
	v_pk_mul_f32 v[108:109], v[48:49], v[48:49]
	v_pk_add_f32 v[106:107], v[106:107], v[106:107] op_sel:[0,1] op_sel_hi:[1,0]
	v_pk_mov_b32 v[112:113], v[110:111], v[108:109] op_sel:[1,0]
	v_mov_b32_e32 v111, v109
	v_pk_add_f32 v[108:109], v[112:113], v[110:111]
	s_waitcnt vmcnt(11)
	v_mul_f32_e32 v110, v38, v38
	v_mul_f32_e32 v111, v39, v39
	v_pk_add_f32 v[108:109], v[108:109], v[108:109] op_sel:[0,1] op_sel_hi:[1,0]
	v_mov_b32_e32 v107, v110
	v_mov_b32_e32 v109, v111
	v_pk_add_f32 v[106:107], v[106:107], v[108:109]
	v_mul_f32_e32 v108, v43, v43
	v_mul_f32_e32 v110, v45, v45
	v_mul_f32_e32 v112, v40, v40
	v_mul_f32_e32 v113, v41, v41
	v_pk_fma_f32 v[108:109], v[42:43], v[42:43], v[108:109] op_sel_hi:[1,1,0]
	v_pk_fma_f32 v[110:111], v[44:45], v[44:45], v[110:111] op_sel_hi:[1,1,0]
	v_mov_b32_e32 v109, v112
	v_mov_b32_e32 v111, v113
	v_pk_add_f32 v[108:109], v[108:109], v[110:111]
	s_waitcnt vmcnt(10)
	v_pk_mul_f32 v[110:111], v[34:35], v[34:35]
	v_pk_add_f32 v[106:107], v[106:107], v[108:109]
	v_pk_mul_f32 v[108:109], v[36:37], v[36:37]
	v_pk_add_f32 v[106:107], v[106:107], v[106:107] op_sel:[0,1] op_sel_hi:[1,0]
	v_pk_mov_b32 v[112:113], v[110:111], v[108:109] op_sel:[1,0]
	v_mov_b32_e32 v111, v109
	v_pk_add_f32 v[108:109], v[112:113], v[110:111]
	s_waitcnt vmcnt(8)
	v_mul_f32_e32 v110, v98, v98
	v_mul_f32_e32 v111, v99, v99
	v_pk_add_f32 v[108:109], v[108:109], v[108:109] op_sel:[0,1] op_sel_hi:[1,0]
	v_mov_b32_e32 v107, v110
	v_mov_b32_e32 v109, v111
	v_pk_add_f32 v[106:107], v[106:107], v[108:109]
	v_mul_f32_e32 v108, v103, v103
	v_mul_f32_e32 v110, v105, v105
	v_mul_f32_e32 v112, v100, v100
	v_mul_f32_e32 v113, v101, v101
	v_pk_fma_f32 v[108:109], v[102:103], v[102:103], v[108:109] op_sel_hi:[1,1,0]
	v_pk_fma_f32 v[110:111], v[104:105], v[104:105], v[110:111] op_sel_hi:[1,1,0]
	v_mov_b32_e32 v109, v112
	v_mov_b32_e32 v111, v113
	v_pk_add_f32 v[108:109], v[108:109], v[110:111]
	v_pk_mul_f32 v[92:93], v[92:93], v[124:125] op_sel_hi:[1,0]
	v_pk_add_f32 v[106:107], v[106:107], v[108:109]
	v_pk_mul_f32 v[66:67], v[66:67], v[124:125] op_sel_hi:[1,0]
	v_add_f32_e32 v106, v106, v107
	ds_bpermute_b32 v107, v225, v106
	v_pk_mul_f32 v[68:69], v[68:69], v[124:125] op_sel_hi:[1,0]
	v_pk_mul_f32 v[92:93], v[20:21], v[92:93]
	v_pk_mul_f32 v[90:91], v[18:19], v[90:91]
	v_pk_mul_f32 v[68:69], v[16:17], v[68:69]
	s_waitcnt lgkmcnt(0)
	v_add_f32_e32 v107, v106, v107
	ds_bpermute_b32 v108, v230, v107
	v_pk_mul_f32 v[66:67], v[14:15], v[66:67]
	v_cvt_pk_bf16_f32 v106, v90, v91
	v_cvt_pk_bf16_f32 v109, v68, v69
	v_pk_mul_f32 v[62:63], v[62:63], v[124:125] op_sel_hi:[1,0]
	s_waitcnt lgkmcnt(0)
	v_add_f32_e32 v110, v107, v108
	ds_bpermute_b32 v111, v231, v110
	v_cvt_pk_bf16_f32 v107, v92, v93
	v_cvt_pk_bf16_f32 v108, v66, v67
	global_store_dwordx4 v[216:217], v[106:109], off offset:2048
	ds_write_b128 v226, v[90:93] offset:4096
	ds_write_b128 v226, v[66:69] offset:4112
	s_waitcnt lgkmcnt(2)
	v_add_f32_e32 v106, v110, v111
	ds_bpermute_b32 v107, v232, v106
	v_pk_mul_f32 v[64:65], v[64:65], v[124:125] op_sel_hi:[1,0]
	v_pk_mul_f32 v[58:59], v[58:59], v[124:125] op_sel_hi:[1,0]
	v_pk_mul_f32 v[60:61], v[60:61], v[124:125] op_sel_hi:[1,0]
	v_pk_mul_f32 v[64:65], v[24:25], v[64:65]
	s_waitcnt lgkmcnt(0)
	v_add_f32_e32 v66, v106, v107
	ds_bpermute_b32 v67, v233, v66
	v_pk_mul_f32 v[62:63], v[22:23], v[62:63]
	v_pk_mul_f32 v[60:61], v[32:33], v[60:61]
	v_pk_mul_f32 v[58:59], v[30:31], v[58:59]
	v_cvt_pk_bf16_f32 v69, v60, v61
	s_waitcnt lgkmcnt(0)
	v_add_f32_e32 v68, v66, v67
	ds_bpermute_b32 v1, v1, v68
	v_cvt_pk_bf16_f32 v66, v62, v63
	v_cvt_pk_bf16_f32 v67, v64, v65
	s_waitcnt lgkmcnt(0)
	v_add_f32_e32 v1, v68, v1
	v_fmamk_f32 v1, v1, 0x3a000000, v221
	v_mul_f32_e32 v68, 0x4f800000, v1
	v_cmp_gt_f32_e32 vcc, s71, v1
	s_nop 1
	v_cndmask_b32_e32 v1, v1, v68, vcc
	v_sqrt_f32_e32 v90, v1
	v_cvt_pk_bf16_f32 v68, v58, v59
	global_store_dwordx4 v[216:217], v[66:69], off offset:3072
	ds_write_b128 v226, v[62:65] offset:6144
	ds_write_b128 v226, v[58:61] offset:6160
	v_add_u32_e32 v66, -1, v90
	v_fma_f32 v67, -v66, v90, v1
	v_cmp_ge_f32_e64 s[6:7], 0, v67
	v_add_u32_e32 v67, 1, v90
	v_fma_f32 v68, -v67, v90, v1
	v_cndmask_b32_e64 v66, v90, v66, s[6:7]
	v_cmp_lt_f32_e64 s[6:7], 0, v68
	s_nop 1
	v_cndmask_b32_e64 v66, v66, v67, s[6:7]
	v_mul_f32_e32 v67, 0x37800000, v66
	v_cndmask_b32_e32 v66, v66, v67, vcc
	v_cmp_class_f32_e32 vcc, v1, v222
	s_nop 1
	v_cndmask_b32_e32 v1, v66, v1, vcc
	v_div_scale_f32 v66, s[6:7], v1, v1, 1.0
	v_rcp_f32_e32 v67, v66
	s_lshl_b64 s[6:7], s[62:63], 12
	v_lshl_add_u64 v[64:65], v[130:131], 0, s[6:7]
	v_fma_f32 v58, -v66, v67, 1.0
	v_fmac_f32_e32 v67, v58, v67
	v_div_scale_f32 v58, vcc, 1.0, v1, 1.0
	v_mul_f32_e32 v59, v58, v67
	v_fma_f32 v60, -v66, v59, v58
	v_fmac_f32_e32 v59, v60, v67
	v_fma_f32 v58, -v66, v59, v58
	v_div_fmas_f32 v58, v58, v67, v59
	v_div_fixup_f32 v62, v58, v1, 1.0
	v_pk_mul_f32 v[54:55], v[54:55], v[62:63] op_sel_hi:[1,0]
	v_pk_mul_f32 v[56:57], v[56:57], v[62:63] op_sel_hi:[1,0]
	v_pk_mul_f32 v[50:51], v[50:51], v[62:63] op_sel_hi:[1,0]
	v_pk_mul_f32 v[52:53], v[52:53], v[62:63] op_sel_hi:[1,0]
	v_pk_mul_f32 v[56:57], v[28:29], v[56:57]
	v_pk_mul_f32 v[54:55], v[26:27], v[54:55]
	v_pk_mul_f32 v[52:53], v[4:5], v[52:53]
	v_pk_mul_f32 v[50:51], v[2:3], v[50:51]
	v_pk_mul_f32 v[46:47], v[46:47], v[62:63] op_sel_hi:[1,0]
	v_pk_mul_f32 v[48:49], v[48:49], v[62:63] op_sel_hi:[1,0]
	v_pk_mul_f32 v[42:43], v[42:43], v[62:63] op_sel_hi:[1,0]
	v_pk_mul_f32 v[44:45], v[44:45], v[62:63] op_sel_hi:[1,0]
	v_cvt_pk_bf16_f32 v58, v54, v55
	v_cvt_pk_bf16_f32 v59, v56, v57
	v_cvt_pk_bf16_f32 v60, v50, v51
	v_cvt_pk_bf16_f32 v61, v52, v53
	v_add_u32_e32 v1, s34, v122
	v_pk_mul_f32 v[48:49], v[8:9], v[48:49]
	v_pk_mul_f32 v[46:47], v[6:7], v[46:47]
	v_pk_mul_f32 v[44:45], v[12:13], v[44:45]
	v_pk_mul_f32 v[42:43], v[10:11], v[42:43]
	v_pk_mul_f32 v[38:39], v[38:39], v[62:63] op_sel_hi:[1,0]
	v_pk_mul_f32 v[40:41], v[40:41], v[62:63] op_sel_hi:[1,0]
	v_pk_mul_f32 v[34:35], v[34:35], v[62:63] op_sel_hi:[1,0]
	v_pk_mul_f32 v[36:37], v[36:37], v[62:63] op_sel_hi:[1,0]
	global_store_dwordx4 v[64:65], v[58:61], off
	ds_write_b128 v1, v[54:57]
	ds_write_b128 v1, v[50:53] offset:16
	v_cvt_pk_bf16_f32 v50, v46, v47
	v_cvt_pk_bf16_f32 v51, v48, v49
	v_cvt_pk_bf16_f32 v52, v42, v43
	v_cvt_pk_bf16_f32 v53, v44, v45
	v_pk_mul_f32 v[40:41], v[20:21], v[40:41]
	v_pk_mul_f32 v[38:39], v[18:19], v[38:39]
	v_pk_mul_f32 v[36:37], v[16:17], v[36:37]
	v_pk_mul_f32 v[34:35], v[14:15], v[34:35]
	global_store_dwordx4 v[64:65], v[50:53], off offset:1024
	ds_write_b128 v1, v[46:49] offset:2048
	ds_write_b128 v1, v[42:45] offset:2064
	v_cvt_pk_bf16_f32 v42, v38, v39
	v_cvt_pk_bf16_f32 v43, v40, v41
	v_cvt_pk_bf16_f32 v44, v34, v35
	v_cvt_pk_bf16_f32 v45, v36, v37
	global_store_dwordx4 v[64:65], v[42:45], off offset:2048
	ds_write_b128 v1, v[38:41] offset:4096
	ds_write_b128 v1, v[34:37] offset:4112
	v_pk_mul_f32 v[34:35], v[102:103], v[62:63] op_sel_hi:[1,0]
	v_pk_mul_f32 v[36:37], v[104:105], v[62:63] op_sel_hi:[1,0]
	v_pk_mul_f32 v[38:39], v[98:99], v[62:63] op_sel_hi:[1,0]
	v_pk_mul_f32 v[40:41], v[100:101], v[62:63] op_sel_hi:[1,0]
	v_pk_mul_f32 v[36:37], v[24:25], v[36:37]
	v_pk_mul_f32 v[34:35], v[22:23], v[34:35]
	v_pk_mul_f32 v[40:41], v[32:33], v[40:41]
	v_pk_mul_f32 v[38:39], v[30:31], v[38:39]
	v_cvt_pk_bf16_f32 v42, v34, v35
	v_cvt_pk_bf16_f32 v43, v36, v37
	v_cvt_pk_bf16_f32 v44, v38, v39
	v_cvt_pk_bf16_f32 v45, v40, v41
	global_store_dwordx4 v[64:65], v[42:45], off offset:3072
	ds_write_b128 v1, v[34:37] offset:6144
	ds_write_b128 v1, v[38:41] offset:6160
	s_waitcnt lgkmcnt(0)
	s_barrier
	v_add_u32_e32 v216, 0x1800, v255
	global_load_dwordx4 v[132:135], v216, s[94:95]
	v_add_u32_e32 v216, 0x1900, v255
	global_load_dwordx4 v[136:139], v216, s[94:95]
	v_add_u32_e32 v216, 0x1a00, v255
	global_load_dwordx4 v[140:143], v216, s[94:95]
	v_add_u32_e32 v216, 0x2400, v255
	global_load_dwordx4 v[144:147], v216, s[94:95]
	v_add_u32_e32 v216, 0x2500, v255
	global_load_dwordx4 v[148:151], v216, s[94:95]
	v_add_u32_e32 v216, 0x2600, v255
	global_load_dwordx4 v[152:155], v216, s[94:95]
	v_add_u32_e32 v216, 0x3000, v255
	global_load_dwordx4 v[156:159], v216, s[94:95]
	v_add_u32_e32 v216, 0x3100, v255
	global_load_dwordx4 v[160:163], v216, s[94:95]
	v_add_u32_e32 v216, 0x3200, v255
	global_load_dwordx4 v[164:167], v216, s[94:95]
	v_add_u32_e32 v216, 0x3c00, v255
	global_load_dwordx4 v[168:171], v216, s[94:95]
	v_add_u32_e32 v216, 0x3d00, v255
	global_load_dwordx4 v[172:175], v216, s[94:95]
	v_add_u32_e32 v216, 0x3e00, v255
	global_load_dwordx4 v[176:179], v216, s[94:95]
	v_add_u32_e32 v216, 0x4800, v255
	global_load_dwordx4 v[180:183], v216, s[94:95]
	v_add_u32_e32 v216, 0x4900, v255
	global_load_dwordx4 v[184:187], v216, s[94:95]
	v_add_u32_e32 v216, 0x4a00, v255
	global_load_dwordx4 v[188:191], v216, s[94:95]
	v_add_u32_e32 v216, 0x5400, v255
	global_load_dwordx4 v[192:195], v216, s[94:95]
	v_add_u32_e32 v216, 0x5500, v255
	global_load_dwordx4 v[226:229], v216, s[94:95]
	v_add_u32_e32 v216, 0x5600, v255
	global_load_dwordx4 v[230:233], v216, s[94:95]
	ds_read_b128 v[234:237], v123
	ds_read_b128 v[238:241], v123 offset:64
	s_waitcnt vmcnt(31) lgkmcnt(1)
	v_mfma_f32_16x16x4_f32 v[242:245], v234, v82, 0
	s_waitcnt vmcnt(30)
	v_mfma_f32_16x16x4_f32 v[246:249], v234, v86, 0
	s_waitcnt vmcnt(29)
	v_mfma_f32_16x16x4_f32 v[250:253], v234, v94, 0
	v_mfma_f32_16x16x4_f32 v[242:245], v235, v83, v[242:245]
	v_mfma_f32_16x16x4_f32 v[246:249], v235, v87, v[246:249]
	v_mfma_f32_16x16x4_f32 v[250:253], v235, v95, v[250:253]
	v_mfma_f32_16x16x4_f32 v[242:245], v236, v84, v[242:245]
	v_mfma_f32_16x16x4_f32 v[246:249], v236, v88, v[246:249]
	v_mfma_f32_16x16x4_f32 v[250:253], v236, v96, v[250:253]
	v_mfma_f32_16x16x4_f32 v[82:85], v237, v85, v[242:245]
	v_mfma_f32_16x16x4_f32 v[86:89], v237, v89, v[246:249]
	v_mfma_f32_16x16x4_f32 v[94:97], v237, v97, v[250:253]
	s_waitcnt vmcnt(28) lgkmcnt(0)
	v_mfma_f32_16x16x4_f32 v[82:85], v238, v70, v[82:85]
	s_waitcnt vmcnt(27)
	v_mfma_f32_16x16x4_f32 v[86:89], v238, v74, v[86:89]
	s_waitcnt vmcnt(26)
	v_mfma_f32_16x16x4_f32 v[94:97], v238, v78, v[94:97]
	v_mfma_f32_16x16x4_f32 v[82:85], v239, v71, v[82:85]
	v_mfma_f32_16x16x4_f32 v[86:89], v239, v75, v[86:89]
	v_mfma_f32_16x16x4_f32 v[94:97], v239, v79, v[94:97]
	v_mfma_f32_16x16x4_f32 v[82:85], v240, v72, v[82:85]
	v_mfma_f32_16x16x4_f32 v[86:89], v240, v76, v[86:89]
	v_mfma_f32_16x16x4_f32 v[94:97], v240, v80, v[94:97]
	v_mfma_f32_16x16x4_f32 v[70:73], v241, v73, v[82:85]
	v_mfma_f32_16x16x4_f32 v[74:77], v241, v77, v[86:89]
	s_nop 5
	ds_read_b128 v[82:85], v123 offset:128
	ds_read_b128 v[86:89], v123 offset:192
	v_mfma_f32_16x16x4_f32 v[78:81], v241, v81, v[94:97]
	s_waitcnt vmcnt(17) lgkmcnt(1)
	v_mfma_f32_16x16x4_f32 v[70:73], v82, v132, v[70:73]
	s_waitcnt vmcnt(16)
	v_mfma_f32_16x16x4_f32 v[74:77], v82, v136, v[74:77]
	s_waitcnt vmcnt(15)
	v_mfma_f32_16x16x4_f32 v[78:81], v82, v140, v[78:81]
	v_mfma_f32_16x16x4_f32 v[70:73], v83, v133, v[70:73]
	v_mfma_f32_16x16x4_f32 v[74:77], v83, v137, v[74:77]
	v_mfma_f32_16x16x4_f32 v[78:81], v83, v141, v[78:81]
	v_mfma_f32_16x16x4_f32 v[70:73], v84, v134, v[70:73]
	v_mfma_f32_16x16x4_f32 v[74:77], v84, v138, v[74:77]
	v_mfma_f32_16x16x4_f32 v[78:81], v84, v142, v[78:81]
	v_mfma_f32_16x16x4_f32 v[132:135], v85, v135, v[70:73]
	v_mfma_f32_16x16x4_f32 v[136:139], v85, v139, v[74:77]
	v_mfma_f32_16x16x4_f32 v[140:143], v85, v143, v[78:81]
	s_waitcnt vmcnt(12) lgkmcnt(0)
	v_mfma_f32_16x16x4_f32 v[140:143], v86, v152, v[140:143]
	v_mfma_f32_16x16x4_f32 v[132:135], v86, v144, v[132:135]
	v_mfma_f32_16x16x4_f32 v[136:139], v86, v148, v[136:139]
	v_mfma_f32_16x16x4_f32 v[140:143], v87, v153, v[140:143]
	v_mfma_f32_16x16x4_f32 v[132:135], v87, v145, v[132:135]
	v_mfma_f32_16x16x4_f32 v[136:139], v87, v149, v[136:139]
	v_mfma_f32_16x16x4_f32 v[140:143], v88, v154, v[140:143]
	v_mfma_f32_16x16x4_f32 v[132:135], v88, v146, v[132:135]
	v_mfma_f32_16x16x4_f32 v[136:139], v88, v150, v[136:139]
	v_mfma_f32_16x16x4_f32 v[132:135], v89, v147, v[132:135]
	v_add_u32_e32 v216, 0x6000, v255
	global_load_dwordx4 v[144:147], v216, s[94:95]
	v_add_u32_e32 v216, 0x6100, v255
	global_load_dwordx4 v[70:73], v216, s[94:95]
	v_add_u32_e32 v216, 0x6200, v255
	global_load_dwordx4 v[74:77], v216, s[94:95]
	v_add_u32_e32 v216, 0x6c00, v255
	global_load_dwordx4 v[78:81], v216, s[94:95]
	v_mfma_f32_16x16x4_f32 v[136:139], v89, v151, v[136:139]
	v_add_u32_e32 v216, 0x6d00, v255
	global_load_dwordx4 v[148:151], v216, s[94:95]
	v_add_u32_e32 v216, 0x6e00, v255
	global_load_dwordx4 v[82:85], v216, s[94:95]
	v_add_u32_e32 v216, 0x7800, v255
	global_load_dwordx4 v[94:97], v216, s[94:95]
	v_add_u32_e32 v216, 0x7900, v255
	global_load_dwordx4 v[234:237], v216, s[94:95]
	v_add_u32_e32 v216, 0x7a00, v255
	global_load_dwordx4 v[238:241], v216, s[94:95]
	v_add_u32_e32 v216, 0x8400, v255
	global_load_dwordx4 v[242:245], v216, s[94:95]
	v_add_u32_e32 v216, 0x8500, v255
	global_load_dwordx4 v[246:249], v216, s[94:95]
	v_add_u32_e32 v216, 0x8600, v255
	global_load_dwordx4 v[250:253], v216, s[94:95]
	v_mfma_f32_16x16x4_f32 v[140:143], v89, v155, v[140:143]
	ds_read_b128 v[152:155], v123 offset:256
	ds_read_b128 v[86:89], v123 offset:320
	s_waitcnt vmcnt(23) lgkmcnt(1)
	v_mfma_f32_16x16x4_f32 v[132:135], v152, v156, v[132:135]
	s_waitcnt vmcnt(22)
	v_mfma_f32_16x16x4_f32 v[136:139], v152, v160, v[136:139]
	s_waitcnt vmcnt(21)
	v_mfma_f32_16x16x4_f32 v[140:143], v152, v164, v[140:143]
	v_mfma_f32_16x16x4_f32 v[132:135], v153, v157, v[132:135]
	v_mfma_f32_16x16x4_f32 v[136:139], v153, v161, v[136:139]
	v_mfma_f32_16x16x4_f32 v[140:143], v153, v165, v[140:143]
	v_mfma_f32_16x16x4_f32 v[132:135], v154, v158, v[132:135]
	v_mfma_f32_16x16x4_f32 v[136:139], v154, v162, v[136:139]
	v_mfma_f32_16x16x4_f32 v[140:143], v154, v166, v[140:143]
	v_mfma_f32_16x16x4_f32 v[132:135], v155, v159, v[132:135]
	v_mfma_f32_16x16x4_f32 v[136:139], v155, v163, v[136:139]
	v_mfma_f32_16x16x4_f32 v[140:143], v155, v167, v[140:143]
	ds_read_b128 v[152:155], v123 offset:384
	ds_read_b128 v[156:159], v123 offset:448
	s_waitcnt vmcnt(20) lgkmcnt(2)
	v_mfma_f32_16x16x4_f32 v[132:135], v86, v168, v[132:135]
	s_waitcnt vmcnt(19)
	v_mfma_f32_16x16x4_f32 v[136:139], v86, v172, v[136:139]
	s_waitcnt vmcnt(18)
	v_mfma_f32_16x16x4_f32 v[140:143], v86, v176, v[140:143]
	v_mfma_f32_16x16x4_f32 v[132:135], v87, v169, v[132:135]
	v_mfma_f32_16x16x4_f32 v[136:139], v87, v173, v[136:139]
	v_mfma_f32_16x16x4_f32 v[140:143], v87, v177, v[140:143]
	v_mfma_f32_16x16x4_f32 v[132:135], v88, v170, v[132:135]
	v_mfma_f32_16x16x4_f32 v[136:139], v88, v174, v[136:139]
	v_mfma_f32_16x16x4_f32 v[140:143], v88, v178, v[140:143]
	v_mfma_f32_16x16x4_f32 v[132:135], v89, v171, v[132:135]
	v_mfma_f32_16x16x4_f32 v[136:139], v89, v175, v[136:139]
	v_mfma_f32_16x16x4_f32 v[140:143], v89, v179, v[140:143]
	s_waitcnt vmcnt(17) lgkmcnt(1)
	v_mfma_f32_16x16x4_f32 v[132:135], v152, v180, v[132:135]
	s_waitcnt vmcnt(16)
	v_mfma_f32_16x16x4_f32 v[136:139], v152, v184, v[136:139]
	s_waitcnt vmcnt(15)
	v_mfma_f32_16x16x4_f32 v[140:143], v152, v188, v[140:143]
	v_mfma_f32_16x16x4_f32 v[132:135], v153, v181, v[132:135]
	v_mfma_f32_16x16x4_f32 v[136:139], v153, v185, v[136:139]
	v_mfma_f32_16x16x4_f32 v[140:143], v153, v189, v[140:143]
	v_mfma_f32_16x16x4_f32 v[132:135], v154, v182, v[132:135]
	v_mfma_f32_16x16x4_f32 v[136:139], v154, v186, v[136:139]
	v_mfma_f32_16x16x4_f32 v[140:143], v154, v190, v[140:143]
	v_mfma_f32_16x16x4_f32 v[132:135], v155, v183, v[132:135]
	v_mfma_f32_16x16x4_f32 v[136:139], v155, v187, v[136:139]
	v_mfma_f32_16x16x4_f32 v[140:143], v155, v191, v[140:143]
	v_add_u32_e32 v216, 0x9000, v255
	global_load_dwordx4 v[152:155], v216, s[94:95]
	v_add_u32_e32 v216, 0x9100, v255
	global_load_dwordx4 v[160:163], v216, s[94:95]
	v_add_u32_e32 v216, 0x9200, v255
	global_load_dwordx4 v[164:167], v216, s[94:95]
	v_add_u32_e32 v216, 0x9c00, v255
	global_load_dwordx4 v[86:89], v216, s[94:95]
	s_waitcnt vmcnt(16) lgkmcnt(0)
	v_mfma_f32_16x16x4_f32 v[140:143], v156, v230, v[140:143]
	v_mfma_f32_16x16x4_f32 v[132:135], v156, v192, v[132:135]
	v_mfma_f32_16x16x4_f32 v[136:139], v156, v226, v[136:139]
	v_mfma_f32_16x16x4_f32 v[140:143], v157, v231, v[140:143]
	v_mfma_f32_16x16x4_f32 v[132:135], v157, v193, v[132:135]
	v_mfma_f32_16x16x4_f32 v[136:139], v157, v227, v[136:139]
	v_mfma_f32_16x16x4_f32 v[140:143], v158, v232, v[140:143]
	v_mfma_f32_16x16x4_f32 v[132:135], v158, v194, v[132:135]
	v_mfma_f32_16x16x4_f32 v[136:139], v158, v228, v[136:139]
	v_mfma_f32_16x16x4_f32 v[132:135], v159, v195, v[132:135]
	v_mfma_f32_16x16x4_f32 v[136:139], v159, v229, v[136:139]
	v_add_u32_e32 v216, 0x9d00, v255
	global_load_dwordx4 v[168:171], v216, s[94:95]
	v_add_u32_e32 v216, 0x9e00, v255
	global_load_dwordx4 v[172:175], v216, s[94:95]
	v_add_u32_e32 v216, 0xa800, v255
	global_load_dwordx4 v[176:179], v216, s[94:95]
	v_add_u32_e32 v216, 0xa900, v255
	global_load_dwordx4 v[180:183], v216, s[94:95]
	v_add_u32_e32 v216, 0xaa00, v255
	global_load_dwordx4 v[184:187], v216, s[94:95]
	v_add_u32_e32 v216, 0xb400, v255
	global_load_dwordx4 v[188:191], v216, s[94:95]
	v_add_u32_e32 v216, 0xb500, v255
	global_load_dwordx4 v[192:195], v216, s[94:95]
	v_add_u32_e32 v216, 0xb600, v255
	global_load_dwordx4 v[226:229], v216, s[94:95]
	s_add_i32 s82, s77, 1
	s_min_u32 s82, s82, 3
	s_lshl_b32 s82, s82, 4
	s_add_i32 s82, s76, s82
	s_ashr_i32 s83, s82, 31
	s_lshl_b64 s[82:83], s[82:83], 13
	v_lshl_add_u64 v[98:99], v[128:129], 0, s[82:83]
	s_add_u32 s82, s82, 0x1000
	s_addc_u32 s83, s83, 0
	global_load_dwordx4 v[118:121], v[98:99], off
	global_load_dwordx4 v[114:117], v[98:99], off offset:16
	global_load_dwordx4 v[110:113], v[98:99], off offset:2048
	global_load_dwordx4 v[106:109], v[98:99], off offset:2064
	v_lshl_add_u64 v[100:101], v[128:129], 0, s[82:83]
	s_add_u32 s82, s82, 0x1000
	s_addc_u32 s83, s83, 0
	global_load_dwordx4 v[58:61], v[100:101], off offset:2064
	global_load_dwordx4 v[90:93], v[100:101], off
	global_load_dwordx4 v[66:69], v[100:101], off offset:16
	global_load_dwordx4 v[62:65], v[100:101], off offset:2048
	v_lshl_add_u64 v[98:99], v[128:129], 0, s[82:83]
	s_nop 0
	global_load_dwordx4 v[54:57], v[98:99], off
	global_load_dwordx4 v[50:53], v[98:99], off offset:16
	global_load_dwordx4 v[196:199], v[98:99], off offset:2064
	global_load_dwordx4 v[200:203], v[98:99], off offset:2048
	s_add_u32 s82, s82, 0x1000
	s_addc_u32 s83, s83, 0
	v_lshl_add_u64 v[100:101], v[128:129], 0, s[82:83]
	s_nop 0
	global_load_dwordx4 v[204:207], v[100:101], off
	global_load_dwordx4 v[208:211], v[100:101], off offset:16
	global_load_dwordx4 v[102:105], v[100:101], off offset:2048
	global_load_dwordx4 v[212:215], v[100:101], off offset:2064
	v_mfma_f32_16x16x4_f32 v[140:143], v159, v233, v[140:143]
	ds_read_b128 v[156:159], v123 offset:512
	ds_read_b128 v[230:233], v123 offset:576
	s_waitcnt vmcnt(39) lgkmcnt(1)
	v_mfma_f32_16x16x4_f32 v[132:135], v156, v144, v[132:135]
	s_waitcnt vmcnt(38)
	v_mfma_f32_16x16x4_f32 v[136:139], v156, v70, v[136:139]
	s_waitcnt vmcnt(37)
	v_mfma_f32_16x16x4_f32 v[140:143], v156, v74, v[140:143]
	v_mfma_f32_16x16x4_f32 v[132:135], v157, v145, v[132:135]
	v_mfma_f32_16x16x4_f32 v[136:139], v157, v71, v[136:139]
	v_mfma_f32_16x16x4_f32 v[140:143], v157, v75, v[140:143]
	v_mfma_f32_16x16x4_f32 v[132:135], v158, v146, v[132:135]
	v_mfma_f32_16x16x4_f32 v[136:139], v158, v72, v[136:139]
	v_mfma_f32_16x16x4_f32 v[140:143], v158, v76, v[140:143]
	v_mfma_f32_16x16x4_f32 v[132:135], v159, v147, v[132:135]
	v_mfma_f32_16x16x4_f32 v[136:139], v159, v73, v[136:139]
	v_mfma_f32_16x16x4_f32 v[140:143], v159, v77, v[140:143]
	s_waitcnt vmcnt(36) lgkmcnt(0)
	v_mfma_f32_16x16x4_f32 v[132:135], v230, v78, v[132:135]
	s_waitcnt vmcnt(35)
	v_mfma_f32_16x16x4_f32 v[136:139], v230, v148, v[136:139]
	s_waitcnt vmcnt(34)
	v_mfma_f32_16x16x4_f32 v[140:143], v230, v82, v[140:143]
	v_mfma_f32_16x16x4_f32 v[132:135], v231, v79, v[132:135]
	v_mfma_f32_16x16x4_f32 v[136:139], v231, v149, v[136:139]
	v_mfma_f32_16x16x4_f32 v[140:143], v231, v83, v[140:143]
	v_mfma_f32_16x16x4_f32 v[132:135], v232, v80, v[132:135]
	v_mfma_f32_16x16x4_f32 v[136:139], v232, v150, v[136:139]
	v_mfma_f32_16x16x4_f32 v[140:143], v232, v84, v[140:143]
	v_mfma_f32_16x16x4_f32 v[132:135], v233, v81, v[132:135]
	v_mfma_f32_16x16x4_f32 v[136:139], v233, v151, v[136:139]
	ds_read_b128 v[144:147], v123 offset:640
	ds_read_b128 v[148:151], v123 offset:704
	v_mfma_f32_16x16x4_f32 v[140:143], v233, v85, v[140:143]
	s_waitcnt vmcnt(33) lgkmcnt(1)
	v_mfma_f32_16x16x4_f32 v[132:135], v144, v94, v[132:135]
	s_waitcnt vmcnt(32)
	v_mfma_f32_16x16x4_f32 v[136:139], v144, v234, v[136:139]
	s_waitcnt vmcnt(31)
	v_mfma_f32_16x16x4_f32 v[140:143], v144, v238, v[140:143]
	v_mfma_f32_16x16x4_f32 v[132:135], v145, v95, v[132:135]
	v_mfma_f32_16x16x4_f32 v[136:139], v145, v235, v[136:139]
	v_mfma_f32_16x16x4_f32 v[140:143], v145, v239, v[140:143]
	v_mfma_f32_16x16x4_f32 v[132:135], v146, v96, v[132:135]
	v_mfma_f32_16x16x4_f32 v[136:139], v146, v236, v[136:139]
	v_mfma_f32_16x16x4_f32 v[140:143], v146, v240, v[140:143]
	v_mfma_f32_16x16x4_f32 v[132:135], v147, v97, v[132:135]
	v_mfma_f32_16x16x4_f32 v[136:139], v147, v237, v[136:139]
	v_mfma_f32_16x16x4_f32 v[140:143], v147, v241, v[140:143]
	s_waitcnt vmcnt(30) lgkmcnt(0)
	v_mfma_f32_16x16x4_f32 v[132:135], v148, v242, v[132:135]
	s_waitcnt vmcnt(29)
	v_mfma_f32_16x16x4_f32 v[136:139], v148, v246, v[136:139]
	s_waitcnt vmcnt(28)
	v_mfma_f32_16x16x4_f32 v[140:143], v148, v250, v[140:143]
	v_mfma_f32_16x16x4_f32 v[132:135], v149, v243, v[132:135]
	v_mfma_f32_16x16x4_f32 v[136:139], v149, v247, v[136:139]
	v_mfma_f32_16x16x4_f32 v[140:143], v149, v251, v[140:143]
	v_mfma_f32_16x16x4_f32 v[132:135], v150, v244, v[132:135]
	v_mfma_f32_16x16x4_f32 v[136:139], v150, v248, v[136:139]
	v_mfma_f32_16x16x4_f32 v[140:143], v150, v252, v[140:143]
	v_mfma_f32_16x16x4_f32 v[132:135], v151, v245, v[132:135]
	v_mfma_f32_16x16x4_f32 v[136:139], v151, v249, v[136:139]
	v_mfma_f32_16x16x4_f32 v[140:143], v151, v253, v[140:143]
	ds_read_b128 v[144:147], v123 offset:768
	ds_read_b128 v[148:151], v123 offset:832
	s_waitcnt vmcnt(27) lgkmcnt(1)
	v_mfma_f32_16x16x4_f32 v[132:135], v144, v152, v[132:135]
	s_waitcnt vmcnt(26)
	v_mfma_f32_16x16x4_f32 v[136:139], v144, v160, v[136:139]
	s_waitcnt vmcnt(25)
	v_mfma_f32_16x16x4_f32 v[140:143], v144, v164, v[140:143]
	v_mfma_f32_16x16x4_f32 v[132:135], v145, v153, v[132:135]
	v_mfma_f32_16x16x4_f32 v[136:139], v145, v161, v[136:139]
	v_mfma_f32_16x16x4_f32 v[140:143], v145, v165, v[140:143]
	v_mfma_f32_16x16x4_f32 v[132:135], v146, v154, v[132:135]
	v_mfma_f32_16x16x4_f32 v[136:139], v146, v162, v[136:139]
	v_mfma_f32_16x16x4_f32 v[140:143], v146, v166, v[140:143]
	v_mfma_f32_16x16x4_f32 v[132:135], v147, v155, v[132:135]
	v_mfma_f32_16x16x4_f32 v[136:139], v147, v163, v[136:139]
	v_mfma_f32_16x16x4_f32 v[140:143], v147, v167, v[140:143]
	s_waitcnt vmcnt(24) lgkmcnt(0)
	v_mfma_f32_16x16x4_f32 v[132:135], v148, v86, v[132:135]
	s_waitcnt vmcnt(23)
	v_mfma_f32_16x16x4_f32 v[136:139], v148, v168, v[136:139]
	s_waitcnt vmcnt(22)
	v_mfma_f32_16x16x4_f32 v[140:143], v148, v172, v[140:143]
	v_mfma_f32_16x16x4_f32 v[132:135], v149, v87, v[132:135]
	v_mfma_f32_16x16x4_f32 v[136:139], v149, v169, v[136:139]
	v_mfma_f32_16x16x4_f32 v[140:143], v149, v173, v[140:143]
	v_mfma_f32_16x16x4_f32 v[132:135], v150, v88, v[132:135]
	v_mfma_f32_16x16x4_f32 v[136:139], v150, v170, v[136:139]
	v_mfma_f32_16x16x4_f32 v[140:143], v150, v174, v[140:143]
	v_mfma_f32_16x16x4_f32 v[132:135], v151, v89, v[132:135]
	v_mfma_f32_16x16x4_f32 v[136:139], v151, v171, v[136:139]
	v_mfma_f32_16x16x4_f32 v[140:143], v151, v175, v[140:143]
	ds_read_b128 v[144:147], v123 offset:896
	ds_read_b128 v[148:151], v123 offset:960
	s_waitcnt vmcnt(21) lgkmcnt(1)
	v_mfma_f32_16x16x4_f32 v[132:135], v144, v176, v[132:135]
	s_waitcnt vmcnt(20)
	v_mfma_f32_16x16x4_f32 v[136:139], v144, v180, v[136:139]
	s_waitcnt vmcnt(19)
	v_mfma_f32_16x16x4_f32 v[140:143], v144, v184, v[140:143]
	v_mfma_f32_16x16x4_f32 v[132:135], v145, v177, v[132:135]
	v_mfma_f32_16x16x4_f32 v[136:139], v145, v181, v[136:139]
	v_mfma_f32_16x16x4_f32 v[140:143], v145, v185, v[140:143]
	v_mfma_f32_16x16x4_f32 v[132:135], v146, v178, v[132:135]
	v_mfma_f32_16x16x4_f32 v[136:139], v146, v182, v[136:139]
	v_mfma_f32_16x16x4_f32 v[140:143], v146, v186, v[140:143]
	v_mfma_f32_16x16x4_f32 v[132:135], v147, v179, v[132:135]
	v_mfma_f32_16x16x4_f32 v[136:139], v147, v183, v[136:139]
	v_mfma_f32_16x16x4_f32 v[140:143], v147, v187, v[140:143]
	s_waitcnt vmcnt(18) lgkmcnt(0)
	v_mfma_f32_16x16x4_f32 v[132:135], v148, v188, v[132:135]
	s_waitcnt vmcnt(17)
	v_mfma_f32_16x16x4_f32 v[136:139], v148, v192, v[136:139]
	s_waitcnt vmcnt(16)
	v_mfma_f32_16x16x4_f32 v[140:143], v148, v226, v[140:143]
	v_mfma_f32_16x16x4_f32 v[132:135], v149, v189, v[132:135]
	v_mfma_f32_16x16x4_f32 v[136:139], v149, v193, v[136:139]
	v_mfma_f32_16x16x4_f32 v[140:143], v149, v227, v[140:143]
	v_mfma_f32_16x16x4_f32 v[132:135], v150, v190, v[132:135]
	v_mfma_f32_16x16x4_f32 v[136:139], v150, v194, v[136:139]
	v_mfma_f32_16x16x4_f32 v[140:143], v150, v228, v[140:143]
	v_mfma_f32_16x16x4_f32 v[132:135], v151, v191, v[132:135]
	v_mfma_f32_16x16x4_f32 v[136:139], v151, v195, v[136:139]
	v_mfma_f32_16x16x4_f32 v[140:143], v151, v229, v[140:143]
	s_nop 8
	ds_write2_b32 v223, v132, v136 offset1:16
	ds_write2_b32 v223, v140, v133 offset0:32 offset1:48
	ds_write2_b32 v223, v137, v141 offset0:64 offset1:80
	ds_write2_b32 v223, v134, v138 offset0:96 offset1:112
	ds_write2_b32 v223, v142, v135 offset0:128 offset1:144
	ds_write2_b32 v223, v139, v143 offset0:160 offset1:176
	s_waitcnt lgkmcnt(0)
	s_barrier
	s_and_saveexec_b64 s[6:7], s[4:5]
	s_cbranch_execz .LBB0_1306
	s_mov_b64 s[8:9], 0
	v_mov_b32_e32 v34, v0
